# gate/up GEMM: SwiGLU bias vectors loaded at the top of the unit's last K-iteration into spare VGPRs; epilogue starts without any VMEM wait; on top of state-pass stack
# baseline (speedup 1.0000x reference)
; #define PG8_SCHED __builtin_amdgcn_sched_barrier(0)
; #define PG8_STAGE_A(b, h, p) do { if constexpr (GATHER) { if ((h) == 0) PG8_STAGE(PG8_SA(b, h), p, vA0); else PG8_STAGE(PG8_SA(b, h), p, vA1); } else PG8_STAGE(PG8_SA(b, h), (p) + ((h) ? hstepA : (size_t)0), voffA); } while (0)
; #define PG8_GOFF1(un, h, d) do { int tz_ = tid; asm volatile("" : "+v"(tz_)); _Pragma("unroll") for (int i_ = 0; i_ < 2; ++i_) { int R_, C_; stage_rc(tz_ * 16 + i_ * 8192, R_, C_); \
;         d[i_] = S.gather(un, R_ + (h) * HALF) + (unsigned)C_ * 2u; } } while (0)
; template <class Epi, class Sched, bool ALIGN_EPI = true, bool SP2 = true, bool FP8 = false, bool GATHER = false>
; __device__ __forceinline__ void gemm_phase(LAS unsigned char* lds, const Dims g, const Sched& S, const Epi& E, const int wv) {
;     ...
;             if constexpr (SP2) {
;             if constexpr (GATHER) { if (last) PG8_GOFF1(un_, 0, vA0); }
;             PG8_LDB(B0, 0, 0); PG8_LDB(B1, 0, 1); PG8_SCHED; PG8_LDA(At, 0, 0); PG8_STAGE_A(1, 1, a1);
;             if constexpr (GATHER) { if (last) PG8_GOFF1(un_, 1, vA1); }
;     __device__ __forceinline__ void operator()(const f32x4 (&acc)[2][2][4][2], const Unit& u, int wr, int wc, int fr, int fq) const {
;         const int row0 = u.pm * BM + wr * 64 + fr, c0 = u.pn * HALF + wc * 32 + 8 * fq;
;         const float* bp = bgu + (size_t)u.aux * 2048 + c0;
;         const f32x4 bg0 = *(const f32x4*)(bp), bg1 = *(const f32x4*)(bp + 4), bu0 = *(const f32x4*)(bp + 1024), bu1 = *(const f32x4*)(bp + 1028);
.LBB0_1427:
	s_cmp_eq_u32 s84, 4
	s_cselect_b64 s[42:43], -1, 0
	s_cmp_lg_u32 s84, 4
	s_cbranch_scc1 .LBB0_1429
	v_lshrrev_b32_e32 v228, 1, v192
	s_lshl_b32 s98, s36, 7
	v_and_or_b32 v228, v228, 24, s98
	v_or_b32_e32 v228, s64, v228
	s_ashr_i32 s101, s38, 31
	s_mov_b32 s100, s38
	s_lshl_b64 s[100:101], s[100:101], 13
	s_add_u32 s100, s4, s100
	s_addc_u32 s101, s5, s101
	v_ashrrev_i32_e32 v229, 31, v228
	v_lshl_add_u64 v[230:231], v[228:229], 2, s[100:101]
	global_load_dwordx4 v[212:215], v[230:231], off
	global_load_dwordx4 v[216:219], v[230:231], off offset:16
	v_lshl_add_u64 v[230:231], v[230:231], 0, s[20:21]
	global_load_dwordx4 v[220:223], v[230:231], off
	global_load_dwordx4 v[224:227], v[230:231], off offset:16
	v_mov_b32_e32 v0, v192
	s_nop 0
	v_ashrrev_i32_e32 v2, 31, v0
	v_lshrrev_b32_e32 v2, 26, v2
	v_lshlrev_b32_e32 v1, 4, v0
	v_add_u32_e32 v2, v0, v2
	v_bfe_i32 v0, v0, 27, 1
	v_lshrrev_b32_e32 v0, 22, v0
	v_add_u32_e32 v0, v1, v0
	v_and_b32_e32 v0, 0xfffffc00, v0
	v_sub_u32_e32 v0, v1, v0
	v_lshrrev_b32_e32 v3, 4, v0
	v_bitop3_b32 v0, v3, v0, 32 bitop3:0x6c
	v_ashrrev_i32_e32 v3, 31, v0
	v_lshrrev_b32_e32 v3, 26, v3
	v_ashrrev_i32_e32 v2, 6, v2
	v_add_u32_e32 v3, v0, v3
	v_ashrrev_i32_e32 v4, 6, v3
	v_lshlrev_b32_e32 v2, 5, v2
	v_and_b32_e32 v3, 0xc0, v3
	v_and_b32_e32 v5, 32, v2
	v_sub_u32_e32 v0, v0, v3
	v_lshlrev_b32_e32 v3, 2, v4
	v_and_b32_e32 v2, 0xffffffc0, v2
	v_add_u32_e32 v1, 0x2000, v1
	v_add3_u32 v2, s81, v3, v2
	v_ashrrev_i32_e32 v3, 31, v1
	v_lshrrev_b32_e32 v3, 22, v3
	v_add_u32_e32 v3, v1, v3
	v_ashrrev_i32_e32 v3, 10, v3
	v_mul_i32_i24_e32 v4, 0x400, v3
	v_sub_u32_e32 v1, v1, v4
	v_lshrrev_b32_e32 v4, 4, v1
	v_bitop3_b32 v1, v4, v1, 32 bitop3:0x6c
	v_ashrrev_i32_e32 v4, 31, v1
	v_lshrrev_b32_e32 v4, 26, v4
	v_ashrrev_i16_sdwa v0, v193, sext(v0) dst_sel:DWORD dst_unused:UNUSED_PAD src0_sel:DWORD src1_sel:BYTE_0
	ds_read_b32 v2, v2
	v_add_u32_e32 v4, v1, v4
	v_add_u32_sdwa v0, v5, sext(v0) dst_sel:DWORD dst_unused:UNUSED_PAD src0_sel:DWORD src1_sel:WORD_0
	v_ashrrev_i32_e32 v5, 6, v4
	v_lshlrev_b32_e32 v3, 5, v3
	v_lshlrev_b32_e32 v5, 2, v5
	v_and_b32_e32 v6, 0xffffffc0, v3
	v_add3_u32 v5, s81, v5, v6
	ds_read_b32 v5, v5
	s_waitcnt lgkmcnt(1)
	v_lshl_add_u32 v194, v0, 1, v2
	v_and_b32_e32 v2, 0xc0, v4
	v_sub_u32_e32 v1, v1, v2
	v_and_b32_e32 v0, 32, v3
	v_ashrrev_i16_sdwa v1, v193, sext(v1) dst_sel:DWORD dst_unused:UNUSED_PAD src0_sel:DWORD src1_sel:BYTE_0
	v_add_u32_sdwa v0, v0, sext(v1) dst_sel:DWORD dst_unused:UNUSED_PAD src0_sel:DWORD src1_sel:WORD_0
	s_waitcnt lgkmcnt(0)
	v_lshl_add_u32 v196, v0, 1, v5

; __device__ __forceinline__ unsigned pk4_fp8(float a, float b, float c, float d) { int w = __builtin_amdgcn_cvt_pk_fp8_f32(a, b, 0, false); w = __builtin_amdgcn_cvt_pk_fp8_f32(c, d, w, true); return (unsigned)w; }
;     __device__ __forceinline__ void operator()(const f32x4 (&acc)[2][2][4][2], const Unit& u, int wr, int wc, int fr, int fq) const {
;         const int row0 = u.pm * BM + wr * 64 + fr, c0 = u.pn * HALF + wc * 32 + 8 * fq;
;         const float* bp = bgu + (size_t)u.aux * 2048 + c0;
;         const f32x4 bg0 = *(const f32x4*)(bp), bg1 = *(const f32x4*)(bp + 4), bu0 = *(const f32x4*)(bp + 1024), bu1 = *(const f32x4*)(bp + 1028);
; #pragma unroll
;         for (int ai = 0; ai < 2; ++ai)
; #pragma unroll
;             for (int mp = 0; mp < 2; ++mp) {
;                 u32x2 wq[2];
; #pragma unroll
;                 for (int mi = 0; mi < 2; ++mi) { const int m = 2 * mp + mi;
;                     const f32x4 g0 = acc[ai][0][m][0] * ascale + bg0, g1 = acc[ai][0][m][1] * ascale + bg1, u0 = acc[ai][1][m][0] * ascale + bu0, u1 = acc[ai][1][m][1] * ascale + bu1;
;                     float r[8];
; #pragma unroll
;                     for (int j = 0; j < 4; ++j) {
;                         float gg = fminf(g0[j], 7.f), uu = fminf(fmaxf(u0[j], -7.f), 7.f); r[j] = 4.f * (uu + 1.f) * gg * __builtin_amdgcn_rcpf(1.f + __expf(-1.702f * gg));
;                         gg = fminf(g1[j], 7.f); uu = fminf(fmaxf(u1[j], -7.f), 7.f); r[4 + j] = 4.f * (uu + 1.f) * gg * __builtin_amdgcn_rcpf(1.f + __expf(-1.702f * gg));
;                     }
;                     wq[mi].x = pk4_fp8(r[0], r[1], r[2], r[3]); wq[mi].y = pk4_fp8(r[4], r[5], r[6], r[7]); }
;                 *(u32x4*)(act + (size_t)(row0 + ai * HALF + (2 * mp + (fq & 1)) * 16) * EFF + (c0 - 8 * (fq & 1))) = widen16(wq[0], wq[1]);
.LBB0_1433:
	v_mov_b32_e32 v18, v192
	s_lshl_b32 s36, s36, 7
	v_lshrrev_b32_e32 v0, 1, v18
	s_ashr_i32 s39, s38, 31
	s_lshl_b32 s40, s77, 8
	v_and_or_b32 v0, v0, 24, s36
	s_lshl_b64 s[38:39], s[38:39], 13
	v_or_b32_e32 v16, s64, v0
	s_add_u32 s38, s4, s38
	s_addc_u32 s39, s5, s39
	v_ashrrev_i32_e32 v17, 31, v16
	v_lshl_add_u64 v[0:1], v[16:17], 2, s[38:39]
	v_add_co_u32_e32 v2, vcc, s73, v0
	v_bfe_u32 v17, v18, 4, 1
	s_nop 0
	v_addc_co_u32_e32 v3, vcc, 0, v1, vcc
	v_lshl_add_u64 v[0:1], v[0:1], 0, s[20:21]
	v_lshlrev_b32_e32 v19, 3, v17
	v_sub_u32_e32 v16, v16, v19
	s_add_i32 s40, s40, s63
	v_and_or_b32 v18, v18, 15, s40
	v_lshl_or_b32 v18, v17, 4, v18
	v_ashrrev_i32_e32 v17, 31, v16
	s_andn2_b64 vcc, exec, s[26:27]
	s_mov_b64 s[26:27], -1
	s_mov_b32 s98, 0x3a000000
	s_mov_b32 s99, 0xbfd9db23
	s_mov_b32 s100, 0x3fb8aa3b
	s_mov_b32 s101, 0
	v_ashrrev_i32_e32 v19, 31, v18
	v_lshlrev_b64 v[48:49], 10, v[18:19]
	v_lshl_add_u64 v[48:49], s[12:13], 0, v[48:49]
	v_lshl_add_u64 v[48:49], v[48:49], 0, v[16:17]
	v_mov_b32_e32 v52, 0x8000
	v_mov_b32_e32 v53, 0
	v_mov_b32_e32 v54, 0x20000
	v_mov_b32_e32 v55, 0
	v_pk_fma_f32 v[24:25], v[188:189], s[98:99], v[212:213] op_sel_hi:[1,0,1]
	v_pk_fma_f32 v[26:27], v[190:191], s[98:99], v[214:215] op_sel_hi:[1,0,1]
	v_pk_fma_f32 v[28:29], v[184:185], s[98:99], v[216:217] op_sel_hi:[1,0,1]
	v_pk_fma_f32 v[30:31], v[186:187], s[98:99], v[218:219] op_sel_hi:[1,0,1]
	v_pk_fma_f32 v[40:41], v[180:181], s[98:99], v[220:221] op_sel_hi:[1,0,1]
	v_pk_fma_f32 v[42:43], v[182:183], s[98:99], v[222:223] op_sel_hi:[1,0,1]
	v_pk_fma_f32 v[44:45], v[176:177], s[98:99], v[224:225] op_sel_hi:[1,0,1]
	v_pk_fma_f32 v[46:47], v[178:179], s[98:99], v[226:227] op_sel_hi:[1,0,1]
	v_min_f32_e32 v24, 0x40e00000, v24
	v_min_f32_e32 v25, 0x40e00000, v25
	v_min_f32_e32 v26, 0x40e00000, v26
	v_min_f32_e32 v27, 0x40e00000, v27
	v_min_f32_e32 v28, 0x40e00000, v28
	v_min_f32_e32 v29, 0x40e00000, v29
	v_min_f32_e32 v30, 0x40e00000, v30
	v_min_f32_e32 v31, 0x40e00000, v31
	v_med3_f32 v40, v40, s74, v203
	v_med3_f32 v41, v41, s74, v203
	v_med3_f32 v42, v42, s74, v203
	v_med3_f32 v43, v43, s74, v203
	v_med3_f32 v44, v44, s74, v203
	v_med3_f32 v45, v45, s74, v203
	v_med3_f32 v46, v46, s74, v203
	v_med3_f32 v47, v47, s74, v203
	v_pk_mul_f32 v[32:33], v[24:25], s[98:99] op_sel:[0,1] op_sel_hi:[1,1]
	v_pk_mul_f32 v[34:35], v[26:27], s[98:99] op_sel:[0,1] op_sel_hi:[1,1]
	v_pk_mul_f32 v[36:37], v[28:29], s[98:99] op_sel:[0,1] op_sel_hi:[1,1]
	v_pk_mul_f32 v[38:39], v[30:31], s[98:99] op_sel:[0,1] op_sel_hi:[1,1]
	v_pk_mul_f32 v[32:33], v[32:33], s[100:101] op_sel_hi:[1,0]
	v_pk_mul_f32 v[34:35], v[34:35], s[100:101] op_sel_hi:[1,0]
	v_pk_mul_f32 v[36:37], v[36:37], s[100:101] op_sel_hi:[1,0]
	v_pk_mul_f32 v[38:39], v[38:39], s[100:101] op_sel_hi:[1,0]
	v_pk_fma_f32 v[40:41], v[40:41], 4.0, 4.0 op_sel_hi:[1,0,0]
	v_pk_fma_f32 v[42:43], v[42:43], 4.0, 4.0 op_sel_hi:[1,0,0]
	v_pk_fma_f32 v[44:45], v[44:45], 4.0, 4.0 op_sel_hi:[1,0,0]
	v_pk_fma_f32 v[46:47], v[46:47], 4.0, 4.0 op_sel_hi:[1,0,0]
	v_exp_f32_e32 v32, v32
	v_exp_f32_e32 v33, v33
	v_exp_f32_e32 v34, v34
	v_exp_f32_e32 v35, v35
	v_exp_f32_e32 v36, v36
	v_exp_f32_e32 v37, v37
	v_exp_f32_e32 v38, v38
	v_exp_f32_e32 v39, v39
	v_pk_mul_f32 v[40:41], v[24:25], v[40:41]
	v_pk_mul_f32 v[42:43], v[26:27], v[42:43]
	v_pk_mul_f32 v[44:45], v[28:29], v[44:45]
	v_pk_mul_f32 v[46:47], v[30:31], v[46:47]
	v_pk_add_f32 v[32:33], v[32:33], 1.0 op_sel_hi:[1,0]
	v_pk_add_f32 v[34:35], v[34:35], 1.0 op_sel_hi:[1,0]
	v_pk_add_f32 v[36:37], v[36:37], 1.0 op_sel_hi:[1,0]
	v_pk_add_f32 v[38:39], v[38:39], 1.0 op_sel_hi:[1,0]
	v_rcp_f32_e32 v32, v32
	v_rcp_f32_e32 v33, v33
	v_rcp_f32_e32 v34, v34
	v_rcp_f32_e32 v35, v35
	v_rcp_f32_e32 v36, v36
	v_rcp_f32_e32 v37, v37
	v_rcp_f32_e32 v38, v38
	v_rcp_f32_e32 v39, v39
	v_pk_mul_f32 v[40:41], v[32:33], v[40:41]
	v_pk_mul_f32 v[42:43], v[34:35], v[42:43]
	v_pk_mul_f32 v[44:45], v[36:37], v[44:45]
	v_pk_mul_f32 v[46:47], v[38:39], v[46:47]
	v_cvt_pk_fp8_f32 v20, v40, v41
	v_cvt_pk_fp8_f32 v21, v44, v45
	v_cvt_pk_fp8_f32 v20, v42, v43 op_sel:[0,0,1]
	v_cvt_pk_fp8_f32 v21, v46, v47 op_sel:[0,0,1]
	v_pk_fma_f32 v[24:25], v[172:173], s[98:99], v[212:213] op_sel_hi:[1,0,1]
	v_pk_fma_f32 v[26:27], v[174:175], s[98:99], v[214:215] op_sel_hi:[1,0,1]
	v_pk_fma_f32 v[28:29], v[168:169], s[98:99], v[216:217] op_sel_hi:[1,0,1]
	v_pk_fma_f32 v[30:31], v[170:171], s[98:99], v[218:219] op_sel_hi:[1,0,1]
	v_pk_fma_f32 v[40:41], v[164:165], s[98:99], v[220:221] op_sel_hi:[1,0,1]
	v_pk_fma_f32 v[42:43], v[166:167], s[98:99], v[222:223] op_sel_hi:[1,0,1]
	v_pk_fma_f32 v[44:45], v[160:161], s[98:99], v[224:225] op_sel_hi:[1,0,1]
	v_pk_fma_f32 v[46:47], v[162:163], s[98:99], v[226:227] op_sel_hi:[1,0,1]
	v_min_f32_e32 v24, 0x40e00000, v24
	v_min_f32_e32 v25, 0x40e00000, v25
	v_min_f32_e32 v26, 0x40e00000, v26
	v_min_f32_e32 v27, 0x40e00000, v27
	v_min_f32_e32 v28, 0x40e00000, v28
	v_min_f32_e32 v29, 0x40e00000, v29
	v_min_f32_e32 v30, 0x40e00000, v30
	v_min_f32_e32 v31, 0x40e00000, v31
	v_med3_f32 v40, v40, s74, v203
	v_med3_f32 v41, v41, s74, v203
	v_med3_f32 v42, v42, s74, v203
	v_med3_f32 v43, v43, s74, v203
	v_med3_f32 v44, v44, s74, v203
	v_med3_f32 v45, v45, s74, v203
	v_med3_f32 v46, v46, s74, v203
	v_med3_f32 v47, v47, s74, v203
	v_pk_mul_f32 v[32:33], v[24:25], s[98:99] op_sel:[0,1] op_sel_hi:[1,1]
	v_pk_mul_f32 v[34:35], v[26:27], s[98:99] op_sel:[0,1] op_sel_hi:[1,1]
	v_pk_mul_f32 v[36:37], v[28:29], s[98:99] op_sel:[0,1] op_sel_hi:[1,1]
	v_pk_mul_f32 v[38:39], v[30:31], s[98:99] op_sel:[0,1] op_sel_hi:[1,1]
	v_pk_mul_f32 v[32:33], v[32:33], s[100:101] op_sel_hi:[1,0]
; __device__ __forceinline__ unsigned pk4_fp8(float a, float b, float c, float d) { int w = __builtin_amdgcn_cvt_pk_fp8_f32(a, b, 0, false); w = __builtin_amdgcn_cvt_pk_fp8_f32(c, d, w, true); return (unsigned)w; }
;     __device__ __forceinline__ void operator()(const f32x4 (&acc)[2][2][4][2], const Unit& u, int wr, int wc, int fr, int fq) const {
;     ...
;         for (int ai = 0; ai < 2; ++ai)
; #pragma unroll
;             for (int mp = 0; mp < 2; ++mp) {
;                 u32x2 wq[2];
; #pragma unroll
;                 for (int mi = 0; mi < 2; ++mi) { const int m = 2 * mp + mi;
;                     const f32x4 g0 = acc[ai][0][m][0] * ascale + bg0, g1 = acc[ai][0][m][1] * ascale + bg1, u0 = acc[ai][1][m][0] * ascale + bu0, u1 = acc[ai][1][m][1] * ascale + bu1;
;                     float r[8];
; #pragma unroll
;                     for (int j = 0; j < 4; ++j) {
;                         float gg = fminf(g0[j], 7.f), uu = fminf(fmaxf(u0[j], -7.f), 7.f); r[j] = 4.f * (uu + 1.f) * gg * __builtin_amdgcn_rcpf(1.f + __expf(-1.702f * gg));
;                         gg = fminf(g1[j], 7.f); uu = fminf(fmaxf(u1[j], -7.f), 7.f); r[4 + j] = 4.f * (uu + 1.f) * gg * __builtin_amdgcn_rcpf(1.f + __expf(-1.702f * gg));
;                     }
;                     wq[mi].x = pk4_fp8(r[0], r[1], r[2], r[3]); wq[mi].y = pk4_fp8(r[4], r[5], r[6], r[7]); }
;                 *(u32x4*)(act + (size_t)(row0 + ai * HALF + (2 * mp + (fq & 1)) * 16) * EFF + (c0 - 8 * (fq & 1))) = widen16(wq[0], wq[1]);
;             }
	v_pk_mul_f32 v[34:35], v[34:35], s[100:101] op_sel_hi:[1,0]
	v_pk_mul_f32 v[36:37], v[36:37], s[100:101] op_sel_hi:[1,0]
	v_pk_mul_f32 v[38:39], v[38:39], s[100:101] op_sel_hi:[1,0]
	v_pk_fma_f32 v[40:41], v[40:41], 4.0, 4.0 op_sel_hi:[1,0,0]
	v_pk_fma_f32 v[42:43], v[42:43], 4.0, 4.0 op_sel_hi:[1,0,0]
	v_pk_fma_f32 v[44:45], v[44:45], 4.0, 4.0 op_sel_hi:[1,0,0]
	v_pk_fma_f32 v[46:47], v[46:47], 4.0, 4.0 op_sel_hi:[1,0,0]
	v_exp_f32_e32 v32, v32
	v_exp_f32_e32 v33, v33
	v_exp_f32_e32 v34, v34
	v_exp_f32_e32 v35, v35
	v_exp_f32_e32 v36, v36
	v_exp_f32_e32 v37, v37
	v_exp_f32_e32 v38, v38
	v_exp_f32_e32 v39, v39
	v_pk_mul_f32 v[40:41], v[24:25], v[40:41]
	v_pk_mul_f32 v[42:43], v[26:27], v[42:43]
	v_pk_mul_f32 v[44:45], v[28:29], v[44:45]
	v_pk_mul_f32 v[46:47], v[30:31], v[46:47]
	v_pk_add_f32 v[32:33], v[32:33], 1.0 op_sel_hi:[1,0]
	v_pk_add_f32 v[34:35], v[34:35], 1.0 op_sel_hi:[1,0]
	v_pk_add_f32 v[36:37], v[36:37], 1.0 op_sel_hi:[1,0]
	v_pk_add_f32 v[38:39], v[38:39], 1.0 op_sel_hi:[1,0]
	v_rcp_f32_e32 v32, v32
	v_rcp_f32_e32 v33, v33
	v_rcp_f32_e32 v34, v34
	v_rcp_f32_e32 v35, v35
	v_rcp_f32_e32 v36, v36
	v_rcp_f32_e32 v37, v37
	v_rcp_f32_e32 v38, v38
	v_rcp_f32_e32 v39, v39
	v_pk_mul_f32 v[40:41], v[32:33], v[40:41]
	v_pk_mul_f32 v[42:43], v[34:35], v[42:43]
	v_pk_mul_f32 v[44:45], v[36:37], v[44:45]
	v_pk_mul_f32 v[46:47], v[38:39], v[46:47]
	v_cvt_pk_fp8_f32 v22, v40, v41
	v_cvt_pk_fp8_f32 v23, v44, v45
	v_cvt_pk_fp8_f32 v22, v42, v43 op_sel:[0,0,1]
	v_cvt_pk_fp8_f32 v23, v46, v47 op_sel:[0,0,1]
	v_mov_b64_e32 v[50:51], v[48:49]
	s_nop 1
	v_permlane16_swap_b32_e32 v20, v22
	v_permlane16_swap_b32_e32 v21, v23
	global_store_dwordx4 v[50:51], v[20:23], off
	v_pk_fma_f32 v[24:25], v[156:157], s[98:99], v[212:213] op_sel_hi:[1,0,1]
	v_pk_fma_f32 v[26:27], v[158:159], s[98:99], v[214:215] op_sel_hi:[1,0,1]
	v_pk_fma_f32 v[28:29], v[152:153], s[98:99], v[216:217] op_sel_hi:[1,0,1]
	v_pk_fma_f32 v[30:31], v[154:155], s[98:99], v[218:219] op_sel_hi:[1,0,1]
	v_pk_fma_f32 v[40:41], v[148:149], s[98:99], v[220:221] op_sel_hi:[1,0,1]
	v_pk_fma_f32 v[42:43], v[150:151], s[98:99], v[222:223] op_sel_hi:[1,0,1]
	v_pk_fma_f32 v[44:45], v[144:145], s[98:99], v[224:225] op_sel_hi:[1,0,1]
	v_pk_fma_f32 v[46:47], v[146:147], s[98:99], v[226:227] op_sel_hi:[1,0,1]
	v_min_f32_e32 v24, 0x40e00000, v24
	v_min_f32_e32 v25, 0x40e00000, v25
	v_min_f32_e32 v26, 0x40e00000, v26
	v_min_f32_e32 v27, 0x40e00000, v27
	v_min_f32_e32 v28, 0x40e00000, v28
	v_min_f32_e32 v29, 0x40e00000, v29
	v_min_f32_e32 v30, 0x40e00000, v30
	v_min_f32_e32 v31, 0x40e00000, v31
	v_med3_f32 v40, v40, s74, v203
	v_med3_f32 v41, v41, s74, v203
	v_med3_f32 v42, v42, s74, v203
	v_med3_f32 v43, v43, s74, v203
	v_med3_f32 v44, v44, s74, v203
	v_med3_f32 v45, v45, s74, v203
	v_med3_f32 v46, v46, s74, v203
	v_med3_f32 v47, v47, s74, v203
	v_pk_mul_f32 v[32:33], v[24:25], s[98:99] op_sel:[0,1] op_sel_hi:[1,1]
	v_pk_mul_f32 v[34:35], v[26:27], s[98:99] op_sel:[0,1] op_sel_hi:[1,1]
	v_pk_mul_f32 v[36:37], v[28:29], s[98:99] op_sel:[0,1] op_sel_hi:[1,1]
	v_pk_mul_f32 v[38:39], v[30:31], s[98:99] op_sel:[0,1] op_sel_hi:[1,1]
	v_pk_mul_f32 v[32:33], v[32:33], s[100:101] op_sel_hi:[1,0]
	v_pk_mul_f32 v[34:35], v[34:35], s[100:101] op_sel_hi:[1,0]
	v_pk_mul_f32 v[36:37], v[36:37], s[100:101] op_sel_hi:[1,0]
	v_pk_mul_f32 v[38:39], v[38:39], s[100:101] op_sel_hi:[1,0]
	v_pk_fma_f32 v[40:41], v[40:41], 4.0, 4.0 op_sel_hi:[1,0,0]
	v_pk_fma_f32 v[42:43], v[42:43], 4.0, 4.0 op_sel_hi:[1,0,0]
	v_pk_fma_f32 v[44:45], v[44:45], 4.0, 4.0 op_sel_hi:[1,0,0]
	v_pk_fma_f32 v[46:47], v[46:47], 4.0, 4.0 op_sel_hi:[1,0,0]
	v_exp_f32_e32 v32, v32
	v_exp_f32_e32 v33, v33
	v_exp_f32_e32 v34, v34
	v_exp_f32_e32 v35, v35
	v_exp_f32_e32 v36, v36
	v_exp_f32_e32 v37, v37
	v_exp_f32_e32 v38, v38
	v_exp_f32_e32 v39, v39
	v_pk_mul_f32 v[40:41], v[24:25], v[40:41]
	v_pk_mul_f32 v[42:43], v[26:27], v[42:43]
	v_pk_mul_f32 v[44:45], v[28:29], v[44:45]
	v_pk_mul_f32 v[46:47], v[30:31], v[46:47]
	v_pk_add_f32 v[32:33], v[32:33], 1.0 op_sel_hi:[1,0]
	v_pk_add_f32 v[34:35], v[34:35], 1.0 op_sel_hi:[1,0]
	v_pk_add_f32 v[36:37], v[36:37], 1.0 op_sel_hi:[1,0]
	v_pk_add_f32 v[38:39], v[38:39], 1.0 op_sel_hi:[1,0]
	v_rcp_f32_e32 v32, v32
	v_rcp_f32_e32 v33, v33
	v_rcp_f32_e32 v34, v34
	v_rcp_f32_e32 v35, v35
	v_rcp_f32_e32 v36, v36
	v_rcp_f32_e32 v37, v37
	v_rcp_f32_e32 v38, v38
	v_rcp_f32_e32 v39, v39
	v_pk_mul_f32 v[40:41], v[32:33], v[40:41]
	v_pk_mul_f32 v[42:43], v[34:35], v[42:43]
	v_pk_mul_f32 v[44:45], v[36:37], v[44:45]
	v_pk_mul_f32 v[46:47], v[38:39], v[46:47]
	v_cvt_pk_fp8_f32 v20, v40, v41
	v_cvt_pk_fp8_f32 v21, v44, v45
	v_cvt_pk_fp8_f32 v20, v42, v43 op_sel:[0,0,1]
	v_cvt_pk_fp8_f32 v21, v46, v47 op_sel:[0,0,1]
	v_pk_fma_f32 v[24:25], v[140:141], s[98:99], v[212:213] op_sel_hi:[1,0,1]
	v_pk_fma_f32 v[26:27], v[142:143], s[98:99], v[214:215] op_sel_hi:[1,0,1]
	v_pk_fma_f32 v[28:29], v[136:137], s[98:99], v[216:217] op_sel_hi:[1,0,1]
	v_pk_fma_f32 v[30:31], v[138:139], s[98:99], v[218:219] op_sel_hi:[1,0,1]
	v_pk_fma_f32 v[40:41], v[132:133], s[98:99], v[220:221] op_sel_hi:[1,0,1]
	v_pk_fma_f32 v[42:43], v[134:135], s[98:99], v[222:223] op_sel_hi:[1,0,1]
	v_pk_fma_f32 v[44:45], v[128:129], s[98:99], v[224:225] op_sel_hi:[1,0,1]
	v_pk_fma_f32 v[46:47], v[130:131], s[98:99], v[226:227] op_sel_hi:[1,0,1]
	v_min_f32_e32 v24, 0x40e00000, v24
	v_min_f32_e32 v25, 0x40e00000, v25
	v_min_f32_e32 v26, 0x40e00000, v26
	v_min_f32_e32 v27, 0x40e00000, v27
	v_min_f32_e32 v28, 0x40e00000, v28
	v_min_f32_e32 v29, 0x40e00000, v29
	v_min_f32_e32 v30, 0x40e00000, v30
	v_min_f32_e32 v31, 0x40e00000, v31
	v_med3_f32 v40, v40, s74, v203
; __device__ __forceinline__ unsigned pk4_fp8(float a, float b, float c, float d) { int w = __builtin_amdgcn_cvt_pk_fp8_f32(a, b, 0, false); w = __builtin_amdgcn_cvt_pk_fp8_f32(c, d, w, true); return (unsigned)w; }
;     __device__ __forceinline__ void operator()(const f32x4 (&acc)[2][2][4][2], const Unit& u, int wr, int wc, int fr, int fq) const {
;     ...
;         for (int ai = 0; ai < 2; ++ai)
; #pragma unroll
;             for (int mp = 0; mp < 2; ++mp) {
;                 u32x2 wq[2];
; #pragma unroll
;                 for (int mi = 0; mi < 2; ++mi) { const int m = 2 * mp + mi;
;                     const f32x4 g0 = acc[ai][0][m][0] * ascale + bg0, g1 = acc[ai][0][m][1] * ascale + bg1, u0 = acc[ai][1][m][0] * ascale + bu0, u1 = acc[ai][1][m][1] * ascale + bu1;
;                     float r[8];
; #pragma unroll
;                     for (int j = 0; j < 4; ++j) {
;                         float gg = fminf(g0[j], 7.f), uu = fminf(fmaxf(u0[j], -7.f), 7.f); r[j] = 4.f * (uu + 1.f) * gg * __builtin_amdgcn_rcpf(1.f + __expf(-1.702f * gg));
;                         gg = fminf(g1[j], 7.f); uu = fminf(fmaxf(u1[j], -7.f), 7.f); r[4 + j] = 4.f * (uu + 1.f) * gg * __builtin_amdgcn_rcpf(1.f + __expf(-1.702f * gg));
;                     }
;                     wq[mi].x = pk4_fp8(r[0], r[1], r[2], r[3]); wq[mi].y = pk4_fp8(r[4], r[5], r[6], r[7]); }
;                 *(u32x4*)(act + (size_t)(row0 + ai * HALF + (2 * mp + (fq & 1)) * 16) * EFF + (c0 - 8 * (fq & 1))) = widen16(wq[0], wq[1]);
;             }
	v_med3_f32 v41, v41, s74, v203
	v_med3_f32 v42, v42, s74, v203
	v_med3_f32 v43, v43, s74, v203
	v_med3_f32 v44, v44, s74, v203
	v_med3_f32 v45, v45, s74, v203
	v_med3_f32 v46, v46, s74, v203
	v_med3_f32 v47, v47, s74, v203
	v_pk_mul_f32 v[32:33], v[24:25], s[98:99] op_sel:[0,1] op_sel_hi:[1,1]
	v_pk_mul_f32 v[34:35], v[26:27], s[98:99] op_sel:[0,1] op_sel_hi:[1,1]
	v_pk_mul_f32 v[36:37], v[28:29], s[98:99] op_sel:[0,1] op_sel_hi:[1,1]
	v_pk_mul_f32 v[38:39], v[30:31], s[98:99] op_sel:[0,1] op_sel_hi:[1,1]
	v_pk_mul_f32 v[32:33], v[32:33], s[100:101] op_sel_hi:[1,0]
	v_pk_mul_f32 v[34:35], v[34:35], s[100:101] op_sel_hi:[1,0]
	v_pk_mul_f32 v[36:37], v[36:37], s[100:101] op_sel_hi:[1,0]
	v_pk_mul_f32 v[38:39], v[38:39], s[100:101] op_sel_hi:[1,0]
	v_pk_fma_f32 v[40:41], v[40:41], 4.0, 4.0 op_sel_hi:[1,0,0]
	v_pk_fma_f32 v[42:43], v[42:43], 4.0, 4.0 op_sel_hi:[1,0,0]
	v_pk_fma_f32 v[44:45], v[44:45], 4.0, 4.0 op_sel_hi:[1,0,0]
	v_pk_fma_f32 v[46:47], v[46:47], 4.0, 4.0 op_sel_hi:[1,0,0]
	v_exp_f32_e32 v32, v32
	v_exp_f32_e32 v33, v33
	v_exp_f32_e32 v34, v34
	v_exp_f32_e32 v35, v35
	v_exp_f32_e32 v36, v36
	v_exp_f32_e32 v37, v37
	v_exp_f32_e32 v38, v38
	v_exp_f32_e32 v39, v39
	v_pk_mul_f32 v[40:41], v[24:25], v[40:41]
	v_pk_mul_f32 v[42:43], v[26:27], v[42:43]
	v_pk_mul_f32 v[44:45], v[28:29], v[44:45]
	v_pk_mul_f32 v[46:47], v[30:31], v[46:47]
	v_pk_add_f32 v[32:33], v[32:33], 1.0 op_sel_hi:[1,0]
	v_pk_add_f32 v[34:35], v[34:35], 1.0 op_sel_hi:[1,0]
	v_pk_add_f32 v[36:37], v[36:37], 1.0 op_sel_hi:[1,0]
	v_pk_add_f32 v[38:39], v[38:39], 1.0 op_sel_hi:[1,0]
	v_rcp_f32_e32 v32, v32
	v_rcp_f32_e32 v33, v33
	v_rcp_f32_e32 v34, v34
	v_rcp_f32_e32 v35, v35
	v_rcp_f32_e32 v36, v36
	v_rcp_f32_e32 v37, v37
	v_rcp_f32_e32 v38, v38
	v_rcp_f32_e32 v39, v39
	v_pk_mul_f32 v[40:41], v[32:33], v[40:41]
	v_pk_mul_f32 v[42:43], v[34:35], v[42:43]
	v_pk_mul_f32 v[44:45], v[36:37], v[44:45]
	v_pk_mul_f32 v[46:47], v[38:39], v[46:47]
	v_cvt_pk_fp8_f32 v22, v40, v41
	v_cvt_pk_fp8_f32 v23, v44, v45
	v_cvt_pk_fp8_f32 v22, v42, v43 op_sel:[0,0,1]
	v_cvt_pk_fp8_f32 v23, v46, v47 op_sel:[0,0,1]
	v_lshl_add_u64 v[50:51], v[48:49], 0, v[52:53]
	s_nop 1
	v_permlane16_swap_b32_e32 v20, v22
	v_permlane16_swap_b32_e32 v21, v23
	global_store_dwordx4 v[50:51], v[20:23], off
	v_pk_fma_f32 v[24:25], v[124:125], s[98:99], v[212:213] op_sel_hi:[1,0,1]
	v_pk_fma_f32 v[26:27], v[126:127], s[98:99], v[214:215] op_sel_hi:[1,0,1]
	v_pk_fma_f32 v[28:29], v[120:121], s[98:99], v[216:217] op_sel_hi:[1,0,1]
	v_pk_fma_f32 v[30:31], v[122:123], s[98:99], v[218:219] op_sel_hi:[1,0,1]
	v_pk_fma_f32 v[40:41], v[116:117], s[98:99], v[220:221] op_sel_hi:[1,0,1]
	v_pk_fma_f32 v[42:43], v[118:119], s[98:99], v[222:223] op_sel_hi:[1,0,1]
	v_pk_fma_f32 v[44:45], v[112:113], s[98:99], v[224:225] op_sel_hi:[1,0,1]
	v_pk_fma_f32 v[46:47], v[114:115], s[98:99], v[226:227] op_sel_hi:[1,0,1]
	v_min_f32_e32 v24, 0x40e00000, v24
	v_min_f32_e32 v25, 0x40e00000, v25
	v_min_f32_e32 v26, 0x40e00000, v26
	v_min_f32_e32 v27, 0x40e00000, v27
	v_min_f32_e32 v28, 0x40e00000, v28
	v_min_f32_e32 v29, 0x40e00000, v29
	v_min_f32_e32 v30, 0x40e00000, v30
	v_min_f32_e32 v31, 0x40e00000, v31
	v_med3_f32 v40, v40, s74, v203
	v_med3_f32 v41, v41, s74, v203
	v_med3_f32 v42, v42, s74, v203
	v_med3_f32 v43, v43, s74, v203
	v_med3_f32 v44, v44, s74, v203
	v_med3_f32 v45, v45, s74, v203
	v_med3_f32 v46, v46, s74, v203
	v_med3_f32 v47, v47, s74, v203
	v_pk_mul_f32 v[32:33], v[24:25], s[98:99] op_sel:[0,1] op_sel_hi:[1,1]
	v_pk_mul_f32 v[34:35], v[26:27], s[98:99] op_sel:[0,1] op_sel_hi:[1,1]
	v_pk_mul_f32 v[36:37], v[28:29], s[98:99] op_sel:[0,1] op_sel_hi:[1,1]
	v_pk_mul_f32 v[38:39], v[30:31], s[98:99] op_sel:[0,1] op_sel_hi:[1,1]
	v_pk_mul_f32 v[32:33], v[32:33], s[100:101] op_sel_hi:[1,0]
	v_pk_mul_f32 v[34:35], v[34:35], s[100:101] op_sel_hi:[1,0]
	v_pk_mul_f32 v[36:37], v[36:37], s[100:101] op_sel_hi:[1,0]
	v_pk_mul_f32 v[38:39], v[38:39], s[100:101] op_sel_hi:[1,0]
	v_pk_fma_f32 v[40:41], v[40:41], 4.0, 4.0 op_sel_hi:[1,0,0]
	v_pk_fma_f32 v[42:43], v[42:43], 4.0, 4.0 op_sel_hi:[1,0,0]
	v_pk_fma_f32 v[44:45], v[44:45], 4.0, 4.0 op_sel_hi:[1,0,0]
	v_pk_fma_f32 v[46:47], v[46:47], 4.0, 4.0 op_sel_hi:[1,0,0]
	v_exp_f32_e32 v32, v32
	v_exp_f32_e32 v33, v33
	v_exp_f32_e32 v34, v34
	v_exp_f32_e32 v35, v35
	v_exp_f32_e32 v36, v36
	v_exp_f32_e32 v37, v37
	v_exp_f32_e32 v38, v38
	v_exp_f32_e32 v39, v39
	v_pk_mul_f32 v[40:41], v[24:25], v[40:41]
	v_pk_mul_f32 v[42:43], v[26:27], v[42:43]
	v_pk_mul_f32 v[44:45], v[28:29], v[44:45]
	v_pk_mul_f32 v[46:47], v[30:31], v[46:47]
	v_pk_add_f32 v[32:33], v[32:33], 1.0 op_sel_hi:[1,0]
	v_pk_add_f32 v[34:35], v[34:35], 1.0 op_sel_hi:[1,0]
	v_pk_add_f32 v[36:37], v[36:37], 1.0 op_sel_hi:[1,0]
	v_pk_add_f32 v[38:39], v[38:39], 1.0 op_sel_hi:[1,0]
	v_rcp_f32_e32 v32, v32
	v_rcp_f32_e32 v33, v33
	v_rcp_f32_e32 v34, v34
	v_rcp_f32_e32 v35, v35
	v_rcp_f32_e32 v36, v36
	v_rcp_f32_e32 v37, v37
	v_rcp_f32_e32 v38, v38
	v_rcp_f32_e32 v39, v39
	v_pk_mul_f32 v[40:41], v[32:33], v[40:41]
	v_pk_mul_f32 v[42:43], v[34:35], v[42:43]
	v_pk_mul_f32 v[44:45], v[36:37], v[44:45]
	v_pk_mul_f32 v[46:47], v[38:39], v[46:47]
	v_cvt_pk_fp8_f32 v20, v40, v41
	v_cvt_pk_fp8_f32 v21, v44, v45
	v_cvt_pk_fp8_f32 v20, v42, v43 op_sel:[0,0,1]
	v_cvt_pk_fp8_f32 v21, v46, v47 op_sel:[0,0,1]
	v_pk_fma_f32 v[24:25], v[108:109], s[98:99], v[212:213] op_sel_hi:[1,0,1]
	v_pk_fma_f32 v[26:27], v[110:111], s[98:99], v[214:215] op_sel_hi:[1,0,1]
	v_pk_fma_f32 v[28:29], v[104:105], s[98:99], v[216:217] op_sel_hi:[1,0,1]
	v_pk_fma_f32 v[30:31], v[106:107], s[98:99], v[218:219] op_sel_hi:[1,0,1]
	v_pk_fma_f32 v[40:41], v[100:101], s[98:99], v[220:221] op_sel_hi:[1,0,1]
; __device__ __forceinline__ unsigned pk4_fp8(float a, float b, float c, float d) { int w = __builtin_amdgcn_cvt_pk_fp8_f32(a, b, 0, false); w = __builtin_amdgcn_cvt_pk_fp8_f32(c, d, w, true); return (unsigned)w; }
;     __device__ __forceinline__ void operator()(const f32x4 (&acc)[2][2][4][2], const Unit& u, int wr, int wc, int fr, int fq) const {
;     ...
;         for (int ai = 0; ai < 2; ++ai)
; #pragma unroll
;             for (int mp = 0; mp < 2; ++mp) {
;                 u32x2 wq[2];
; #pragma unroll
;                 for (int mi = 0; mi < 2; ++mi) { const int m = 2 * mp + mi;
;                     const f32x4 g0 = acc[ai][0][m][0] * ascale + bg0, g1 = acc[ai][0][m][1] * ascale + bg1, u0 = acc[ai][1][m][0] * ascale + bu0, u1 = acc[ai][1][m][1] * ascale + bu1;
;                     float r[8];
; #pragma unroll
;                     for (int j = 0; j < 4; ++j) {
;                         float gg = fminf(g0[j], 7.f), uu = fminf(fmaxf(u0[j], -7.f), 7.f); r[j] = 4.f * (uu + 1.f) * gg * __builtin_amdgcn_rcpf(1.f + __expf(-1.702f * gg));
;                         gg = fminf(g1[j], 7.f); uu = fminf(fmaxf(u1[j], -7.f), 7.f); r[4 + j] = 4.f * (uu + 1.f) * gg * __builtin_amdgcn_rcpf(1.f + __expf(-1.702f * gg));
;                     }
;                     wq[mi].x = pk4_fp8(r[0], r[1], r[2], r[3]); wq[mi].y = pk4_fp8(r[4], r[5], r[6], r[7]); }
;                 *(u32x4*)(act + (size_t)(row0 + ai * HALF + (2 * mp + (fq & 1)) * 16) * EFF + (c0 - 8 * (fq & 1))) = widen16(wq[0], wq[1]);
;             }
	v_pk_fma_f32 v[42:43], v[102:103], s[98:99], v[222:223] op_sel_hi:[1,0,1]
	v_pk_fma_f32 v[44:45], v[96:97], s[98:99], v[224:225] op_sel_hi:[1,0,1]
	v_pk_fma_f32 v[46:47], v[98:99], s[98:99], v[226:227] op_sel_hi:[1,0,1]
	v_min_f32_e32 v24, 0x40e00000, v24
	v_min_f32_e32 v25, 0x40e00000, v25
	v_min_f32_e32 v26, 0x40e00000, v26
	v_min_f32_e32 v27, 0x40e00000, v27
	v_min_f32_e32 v28, 0x40e00000, v28
	v_min_f32_e32 v29, 0x40e00000, v29
	v_min_f32_e32 v30, 0x40e00000, v30
	v_min_f32_e32 v31, 0x40e00000, v31
	v_med3_f32 v40, v40, s74, v203
	v_med3_f32 v41, v41, s74, v203
	v_med3_f32 v42, v42, s74, v203
	v_med3_f32 v43, v43, s74, v203
	v_med3_f32 v44, v44, s74, v203
	v_med3_f32 v45, v45, s74, v203
	v_med3_f32 v46, v46, s74, v203
	v_med3_f32 v47, v47, s74, v203
	v_pk_mul_f32 v[32:33], v[24:25], s[98:99] op_sel:[0,1] op_sel_hi:[1,1]
	v_pk_mul_f32 v[34:35], v[26:27], s[98:99] op_sel:[0,1] op_sel_hi:[1,1]
	v_pk_mul_f32 v[36:37], v[28:29], s[98:99] op_sel:[0,1] op_sel_hi:[1,1]
	v_pk_mul_f32 v[38:39], v[30:31], s[98:99] op_sel:[0,1] op_sel_hi:[1,1]
	v_pk_mul_f32 v[32:33], v[32:33], s[100:101] op_sel_hi:[1,0]
	v_pk_mul_f32 v[34:35], v[34:35], s[100:101] op_sel_hi:[1,0]
	v_pk_mul_f32 v[36:37], v[36:37], s[100:101] op_sel_hi:[1,0]
	v_pk_mul_f32 v[38:39], v[38:39], s[100:101] op_sel_hi:[1,0]
	v_pk_fma_f32 v[40:41], v[40:41], 4.0, 4.0 op_sel_hi:[1,0,0]
	v_pk_fma_f32 v[42:43], v[42:43], 4.0, 4.0 op_sel_hi:[1,0,0]
	v_pk_fma_f32 v[44:45], v[44:45], 4.0, 4.0 op_sel_hi:[1,0,0]
	v_pk_fma_f32 v[46:47], v[46:47], 4.0, 4.0 op_sel_hi:[1,0,0]
	v_exp_f32_e32 v32, v32
	v_exp_f32_e32 v33, v33
	v_exp_f32_e32 v34, v34
	v_exp_f32_e32 v35, v35
	v_exp_f32_e32 v36, v36
	v_exp_f32_e32 v37, v37
	v_exp_f32_e32 v38, v38
	v_exp_f32_e32 v39, v39
	v_pk_mul_f32 v[40:41], v[24:25], v[40:41]
	v_pk_mul_f32 v[42:43], v[26:27], v[42:43]
	v_pk_mul_f32 v[44:45], v[28:29], v[44:45]
	v_pk_mul_f32 v[46:47], v[30:31], v[46:47]
	v_pk_add_f32 v[32:33], v[32:33], 1.0 op_sel_hi:[1,0]
	v_pk_add_f32 v[34:35], v[34:35], 1.0 op_sel_hi:[1,0]
	v_pk_add_f32 v[36:37], v[36:37], 1.0 op_sel_hi:[1,0]
	v_pk_add_f32 v[38:39], v[38:39], 1.0 op_sel_hi:[1,0]
	v_rcp_f32_e32 v32, v32
	v_rcp_f32_e32 v33, v33
	v_rcp_f32_e32 v34, v34
	v_rcp_f32_e32 v35, v35
	v_rcp_f32_e32 v36, v36
	v_rcp_f32_e32 v37, v37
	v_rcp_f32_e32 v38, v38
	v_rcp_f32_e32 v39, v39
	v_pk_mul_f32 v[40:41], v[32:33], v[40:41]
	v_pk_mul_f32 v[42:43], v[34:35], v[42:43]
	v_pk_mul_f32 v[44:45], v[36:37], v[44:45]
	v_pk_mul_f32 v[46:47], v[38:39], v[46:47]
	v_cvt_pk_fp8_f32 v22, v40, v41
	v_cvt_pk_fp8_f32 v23, v44, v45
	v_cvt_pk_fp8_f32 v22, v42, v43 op_sel:[0,0,1]
	v_cvt_pk_fp8_f32 v23, v46, v47 op_sel:[0,0,1]
	v_lshl_add_u64 v[50:51], v[48:49], 0, v[54:55]
	s_nop 1
	v_permlane16_swap_b32_e32 v20, v22
	v_permlane16_swap_b32_e32 v21, v23
	global_store_dwordx4 v[50:51], v[20:23], off
	v_pk_fma_f32 v[24:25], v[92:93], s[98:99], v[212:213] op_sel_hi:[1,0,1]
	v_pk_fma_f32 v[26:27], v[94:95], s[98:99], v[214:215] op_sel_hi:[1,0,1]
	v_pk_fma_f32 v[28:29], v[88:89], s[98:99], v[216:217] op_sel_hi:[1,0,1]
	v_pk_fma_f32 v[30:31], v[90:91], s[98:99], v[218:219] op_sel_hi:[1,0,1]
	v_pk_fma_f32 v[40:41], v[84:85], s[98:99], v[220:221] op_sel_hi:[1,0,1]
	v_pk_fma_f32 v[42:43], v[86:87], s[98:99], v[222:223] op_sel_hi:[1,0,1]
	v_pk_fma_f32 v[44:45], v[80:81], s[98:99], v[224:225] op_sel_hi:[1,0,1]
	v_pk_fma_f32 v[46:47], v[82:83], s[98:99], v[226:227] op_sel_hi:[1,0,1]
	v_min_f32_e32 v24, 0x40e00000, v24
	v_min_f32_e32 v25, 0x40e00000, v25
	v_min_f32_e32 v26, 0x40e00000, v26
	v_min_f32_e32 v27, 0x40e00000, v27
	v_min_f32_e32 v28, 0x40e00000, v28
	v_min_f32_e32 v29, 0x40e00000, v29
	v_min_f32_e32 v30, 0x40e00000, v30
	v_min_f32_e32 v31, 0x40e00000, v31
	v_med3_f32 v40, v40, s74, v203
	v_med3_f32 v41, v41, s74, v203
	v_med3_f32 v42, v42, s74, v203
	v_med3_f32 v43, v43, s74, v203
	v_med3_f32 v44, v44, s74, v203
	v_med3_f32 v45, v45, s74, v203
	v_med3_f32 v46, v46, s74, v203
	v_med3_f32 v47, v47, s74, v203
	v_pk_mul_f32 v[32:33], v[24:25], s[98:99] op_sel:[0,1] op_sel_hi:[1,1]
	v_pk_mul_f32 v[34:35], v[26:27], s[98:99] op_sel:[0,1] op_sel_hi:[1,1]
	v_pk_mul_f32 v[36:37], v[28:29], s[98:99] op_sel:[0,1] op_sel_hi:[1,1]
	v_pk_mul_f32 v[38:39], v[30:31], s[98:99] op_sel:[0,1] op_sel_hi:[1,1]
	v_pk_mul_f32 v[32:33], v[32:33], s[100:101] op_sel_hi:[1,0]
	v_pk_mul_f32 v[34:35], v[34:35], s[100:101] op_sel_hi:[1,0]
	v_pk_mul_f32 v[36:37], v[36:37], s[100:101] op_sel_hi:[1,0]
	v_pk_mul_f32 v[38:39], v[38:39], s[100:101] op_sel_hi:[1,0]
	v_pk_fma_f32 v[40:41], v[40:41], 4.0, 4.0 op_sel_hi:[1,0,0]
	v_pk_fma_f32 v[42:43], v[42:43], 4.0, 4.0 op_sel_hi:[1,0,0]
; __device__ __forceinline__ unsigned pk4_fp8(float a, float b, float c, float d) { int w = __builtin_amdgcn_cvt_pk_fp8_f32(a, b, 0, false); w = __builtin_amdgcn_cvt_pk_fp8_f32(c, d, w, true); return (unsigned)w; }
;     __device__ __forceinline__ void operator()(const f32x4 (&acc)[2][2][4][2], const Unit& u, int wr, int wc, int fr, int fq) const {
;     ...
;         for (int ai = 0; ai < 2; ++ai)
; #pragma unroll
;             for (int mp = 0; mp < 2; ++mp) {
;                 u32x2 wq[2];
; #pragma unroll
;                 for (int mi = 0; mi < 2; ++mi) { const int m = 2 * mp + mi;
;                     const f32x4 g0 = acc[ai][0][m][0] * ascale + bg0, g1 = acc[ai][0][m][1] * ascale + bg1, u0 = acc[ai][1][m][0] * ascale + bu0, u1 = acc[ai][1][m][1] * ascale + bu1;
;                     float r[8];
; #pragma unroll
;                     for (int j = 0; j < 4; ++j) {
;                         float gg = fminf(g0[j], 7.f), uu = fminf(fmaxf(u0[j], -7.f), 7.f); r[j] = 4.f * (uu + 1.f) * gg * __builtin_amdgcn_rcpf(1.f + __expf(-1.702f * gg));
;                         gg = fminf(g1[j], 7.f); uu = fminf(fmaxf(u1[j], -7.f), 7.f); r[4 + j] = 4.f * (uu + 1.f) * gg * __builtin_amdgcn_rcpf(1.f + __expf(-1.702f * gg));
;                     }
;                     wq[mi].x = pk4_fp8(r[0], r[1], r[2], r[3]); wq[mi].y = pk4_fp8(r[4], r[5], r[6], r[7]); }
;                 *(u32x4*)(act + (size_t)(row0 + ai * HALF + (2 * mp + (fq & 1)) * 16) * EFF + (c0 - 8 * (fq & 1))) = widen16(wq[0], wq[1]);
;             }
	v_pk_fma_f32 v[44:45], v[44:45], 4.0, 4.0 op_sel_hi:[1,0,0]
	v_pk_fma_f32 v[46:47], v[46:47], 4.0, 4.0 op_sel_hi:[1,0,0]
	v_exp_f32_e32 v32, v32
	v_exp_f32_e32 v33, v33
	v_exp_f32_e32 v34, v34
	v_exp_f32_e32 v35, v35
	v_exp_f32_e32 v36, v36
	v_exp_f32_e32 v37, v37
	v_exp_f32_e32 v38, v38
	v_exp_f32_e32 v39, v39
	v_pk_mul_f32 v[40:41], v[24:25], v[40:41]
	v_pk_mul_f32 v[42:43], v[26:27], v[42:43]
	v_pk_mul_f32 v[44:45], v[28:29], v[44:45]
	v_pk_mul_f32 v[46:47], v[30:31], v[46:47]
	v_pk_add_f32 v[32:33], v[32:33], 1.0 op_sel_hi:[1,0]
	v_pk_add_f32 v[34:35], v[34:35], 1.0 op_sel_hi:[1,0]
	v_pk_add_f32 v[36:37], v[36:37], 1.0 op_sel_hi:[1,0]
	v_pk_add_f32 v[38:39], v[38:39], 1.0 op_sel_hi:[1,0]
	v_rcp_f32_e32 v32, v32
	v_rcp_f32_e32 v33, v33
	v_rcp_f32_e32 v34, v34
	v_rcp_f32_e32 v35, v35
	v_rcp_f32_e32 v36, v36
	v_rcp_f32_e32 v37, v37
	v_rcp_f32_e32 v38, v38
	v_rcp_f32_e32 v39, v39
	v_pk_mul_f32 v[40:41], v[32:33], v[40:41]
	v_pk_mul_f32 v[42:43], v[34:35], v[42:43]
	v_pk_mul_f32 v[44:45], v[36:37], v[44:45]
	v_pk_mul_f32 v[46:47], v[38:39], v[46:47]
	v_cvt_pk_fp8_f32 v20, v40, v41
	v_cvt_pk_fp8_f32 v21, v44, v45
	v_cvt_pk_fp8_f32 v20, v42, v43 op_sel:[0,0,1]
	v_cvt_pk_fp8_f32 v21, v46, v47 op_sel:[0,0,1]
	v_pk_fma_f32 v[24:25], v[76:77], s[98:99], v[212:213] op_sel_hi:[1,0,1]
	v_pk_fma_f32 v[26:27], v[78:79], s[98:99], v[214:215] op_sel_hi:[1,0,1]
	v_pk_fma_f32 v[28:29], v[72:73], s[98:99], v[216:217] op_sel_hi:[1,0,1]
	v_pk_fma_f32 v[30:31], v[74:75], s[98:99], v[218:219] op_sel_hi:[1,0,1]
	v_pk_fma_f32 v[40:41], v[68:69], s[98:99], v[220:221] op_sel_hi:[1,0,1]
	v_pk_fma_f32 v[42:43], v[70:71], s[98:99], v[222:223] op_sel_hi:[1,0,1]
	v_pk_fma_f32 v[44:45], v[64:65], s[98:99], v[224:225] op_sel_hi:[1,0,1]
	v_pk_fma_f32 v[46:47], v[66:67], s[98:99], v[226:227] op_sel_hi:[1,0,1]
	v_min_f32_e32 v24, 0x40e00000, v24
	v_min_f32_e32 v25, 0x40e00000, v25
	v_min_f32_e32 v26, 0x40e00000, v26
	v_min_f32_e32 v27, 0x40e00000, v27
	v_min_f32_e32 v28, 0x40e00000, v28
	v_min_f32_e32 v29, 0x40e00000, v29
	v_min_f32_e32 v30, 0x40e00000, v30
	v_min_f32_e32 v31, 0x40e00000, v31
	v_med3_f32 v40, v40, s74, v203
	v_med3_f32 v41, v41, s74, v203
	v_med3_f32 v42, v42, s74, v203
	v_med3_f32 v43, v43, s74, v203
	v_med3_f32 v44, v44, s74, v203
	v_med3_f32 v45, v45, s74, v203
	v_med3_f32 v46, v46, s74, v203
	v_med3_f32 v47, v47, s74, v203
	v_pk_mul_f32 v[32:33], v[24:25], s[98:99] op_sel:[0,1] op_sel_hi:[1,1]
	v_pk_mul_f32 v[34:35], v[26:27], s[98:99] op_sel:[0,1] op_sel_hi:[1,1]
	v_pk_mul_f32 v[36:37], v[28:29], s[98:99] op_sel:[0,1] op_sel_hi:[1,1]
	v_pk_mul_f32 v[38:39], v[30:31], s[98:99] op_sel:[0,1] op_sel_hi:[1,1]
	v_pk_mul_f32 v[32:33], v[32:33], s[100:101] op_sel_hi:[1,0]
	v_pk_mul_f32 v[34:35], v[34:35], s[100:101] op_sel_hi:[1,0]
	v_pk_mul_f32 v[36:37], v[36:37], s[100:101] op_sel_hi:[1,0]
	v_pk_mul_f32 v[38:39], v[38:39], s[100:101] op_sel_hi:[1,0]
	v_pk_fma_f32 v[40:41], v[40:41], 4.0, 4.0 op_sel_hi:[1,0,0]
	v_pk_fma_f32 v[42:43], v[42:43], 4.0, 4.0 op_sel_hi:[1,0,0]
	v_pk_fma_f32 v[44:45], v[44:45], 4.0, 4.0 op_sel_hi:[1,0,0]
	v_pk_fma_f32 v[46:47], v[46:47], 4.0, 4.0 op_sel_hi:[1,0,0]
	v_exp_f32_e32 v32, v32
	v_exp_f32_e32 v33, v33
	v_exp_f32_e32 v34, v34
	v_exp_f32_e32 v35, v35
	v_exp_f32_e32 v36, v36
	v_exp_f32_e32 v37, v37
	v_exp_f32_e32 v38, v38
	v_exp_f32_e32 v39, v39
	v_pk_mul_f32 v[40:41], v[24:25], v[40:41]
	v_pk_mul_f32 v[42:43], v[26:27], v[42:43]
	v_pk_mul_f32 v[44:45], v[28:29], v[44:45]
	v_pk_mul_f32 v[46:47], v[30:31], v[46:47]
	v_pk_add_f32 v[32:33], v[32:33], 1.0 op_sel_hi:[1,0]
	v_pk_add_f32 v[34:35], v[34:35], 1.0 op_sel_hi:[1,0]
	v_pk_add_f32 v[36:37], v[36:37], 1.0 op_sel_hi:[1,0]
	v_pk_add_f32 v[38:39], v[38:39], 1.0 op_sel_hi:[1,0]
	v_rcp_f32_e32 v32, v32
	v_rcp_f32_e32 v33, v33
	v_rcp_f32_e32 v34, v34
	v_rcp_f32_e32 v35, v35
	v_rcp_f32_e32 v36, v36
	v_rcp_f32_e32 v37, v37
	v_rcp_f32_e32 v38, v38
	v_rcp_f32_e32 v39, v39
	v_pk_mul_f32 v[40:41], v[32:33], v[40:41]
	v_pk_mul_f32 v[42:43], v[34:35], v[42:43]
	v_pk_mul_f32 v[44:45], v[36:37], v[44:45]
	v_pk_mul_f32 v[46:47], v[38:39], v[46:47]
	v_cvt_pk_fp8_f32 v22, v40, v41
	v_cvt_pk_fp8_f32 v23, v44, v45
	v_cvt_pk_fp8_f32 v22, v42, v43 op_sel:[0,0,1]
	v_cvt_pk_fp8_f32 v23, v46, v47 op_sel:[0,0,1]
	v_lshl_add_u64 v[50:51], v[48:49], 0, v[54:55]
	v_lshl_add_u64 v[50:51], v[50:51], 0, v[52:53]
	s_nop 1
	v_permlane16_swap_b32_e32 v20, v22
	v_permlane16_swap_b32_e32 v21, v23
	global_store_dwordx4 v[50:51], v[20:23], off
	s_cbranch_vccnz .LBB0_1419
	s_andn2_b64 vcc, exec, s[14:15]
	s_cbranch_vccnz .LBB0_1418
	s_barrier
	s_branch .LBB0_1418

; #define PG8_SCHED __builtin_amdgcn_sched_barrier(0)
; #define PG8_STAGE_A(b, h, p) do { if constexpr (GATHER) { if ((h) == 0) PG8_STAGE(PG8_SA(b, h), p, vA0); else PG8_STAGE(PG8_SA(b, h), p, vA1); } else PG8_STAGE(PG8_SA(b, h), (p) + ((h) ? hstepA : (size_t)0), voffA); } while (0)
; #define PG8_GOFF1(un, h, d) do { int tz_ = tid; asm volatile("" : "+v"(tz_)); _Pragma("unroll") for (int i_ = 0; i_ < 2; ++i_) { int R_, C_; stage_rc(tz_ * 16 + i_ * 8192, R_, C_); \
;         d[i_] = S.gather(un, R_ + (h) * HALF) + (unsigned)C_ * 2u; } } while (0)
; template <class Epi, class Sched, bool ALIGN_EPI = true, bool SP2 = true, bool FP8 = false, bool GATHER = false>
; __device__ __forceinline__ void gemm_phase(LAS unsigned char* lds, const Dims g, const Sched& S, const Epi& E, const int wv) {
;     ...
;             if constexpr (SP2) {
;             if constexpr (GATHER) { if (last) PG8_GOFF1(un_, 0, vA0); }
;             PG8_LDB(B0, 0, 0); PG8_LDB(B1, 0, 1); PG8_SCHED; PG8_LDA(At, 0, 0); PG8_STAGE_A(1, 1, a1);
;             if constexpr (GATHER) { if (last) PG8_GOFF1(un_, 1, vA1); }
;     __device__ __forceinline__ void operator()(const f32x4 (&acc)[2][2][4][2], const Unit& u, int wr, int wc, int fr, int fq) const {
;         const int row0 = u.pm * BM + wr * 64 + fr, c0 = u.pn * HALF + wc * 32 + 8 * fq;
;         const float* bp = bgu + (size_t)u.aux * 2048 + c0;
;         const f32x4 bg0 = *(const f32x4*)(bp), bg1 = *(const f32x4*)(bp + 4), bu0 = *(const f32x4*)(bp + 1024), bu1 = *(const f32x4*)(bp + 1028);
.LBB0_2531:
	s_cmp_eq_u32 s84, 4
	s_cselect_b64 s[40:41], -1, 0
	s_cmp_lg_u32 s84, 4
	s_cbranch_scc1 .LBB0_2533
	v_lshrrev_b32_e32 v228, 1, v192
	s_lshl_b32 s98, s26, 7
	v_and_or_b32 v228, v228, 24, s98
	v_or_b32_e32 v228, s64, v228
	s_ashr_i32 s101, s36, 31
	s_mov_b32 s100, s36
	s_lshl_b64 s[100:101], s[100:101], 13
	s_add_u32 s100, s61, s100
	s_addc_u32 s101, s62, s101
	v_ashrrev_i32_e32 v229, 31, v228
	v_lshl_add_u64 v[230:231], v[228:229], 2, s[100:101]
	global_load_dwordx4 v[212:215], v[230:231], off
	global_load_dwordx4 v[216:219], v[230:231], off offset:16
	v_lshl_add_u64 v[230:231], v[230:231], 0, s[16:17]
	global_load_dwordx4 v[220:223], v[230:231], off
	global_load_dwordx4 v[224:227], v[230:231], off offset:16
	v_mov_b32_e32 v0, v192
	s_nop 0
	v_ashrrev_i32_e32 v2, 31, v0
	v_lshrrev_b32_e32 v2, 26, v2
	v_lshlrev_b32_e32 v1, 4, v0
	v_add_u32_e32 v2, v0, v2
	v_bfe_i32 v0, v0, 27, 1
	v_lshrrev_b32_e32 v0, 22, v0
	v_add_u32_e32 v0, v1, v0
	v_and_b32_e32 v0, 0xfffffc00, v0
	v_sub_u32_e32 v0, v1, v0
	v_lshrrev_b32_e32 v3, 4, v0
	v_bitop3_b32 v0, v3, v0, 32 bitop3:0x6c
	v_ashrrev_i32_e32 v3, 31, v0
	v_lshrrev_b32_e32 v3, 26, v3
	v_ashrrev_i32_e32 v2, 6, v2
	v_add_u32_e32 v3, v0, v3
	v_ashrrev_i32_e32 v4, 6, v3
	v_lshlrev_b32_e32 v2, 5, v2
	v_and_b32_e32 v3, 0xc0, v3
	v_and_b32_e32 v5, 32, v2
	v_sub_u32_e32 v0, v0, v3
	v_lshlrev_b32_e32 v3, 2, v4
	v_and_b32_e32 v2, 0xffffffc0, v2
	v_add_u32_e32 v1, 0x2000, v1
	v_add3_u32 v2, s81, v3, v2
	v_ashrrev_i32_e32 v3, 31, v1
	v_lshrrev_b32_e32 v3, 22, v3
	v_add_u32_e32 v3, v1, v3
	v_ashrrev_i32_e32 v3, 10, v3
	v_mul_i32_i24_e32 v4, 0x400, v3
	v_sub_u32_e32 v1, v1, v4
	v_lshrrev_b32_e32 v4, 4, v1
	v_bitop3_b32 v1, v4, v1, 32 bitop3:0x6c
	v_ashrrev_i32_e32 v4, 31, v1
	v_lshrrev_b32_e32 v4, 26, v4
	v_ashrrev_i16_sdwa v0, v193, sext(v0) dst_sel:DWORD dst_unused:UNUSED_PAD src0_sel:DWORD src1_sel:BYTE_0
	ds_read_b32 v2, v2
	v_add_u32_e32 v4, v1, v4
	v_add_u32_sdwa v0, v5, sext(v0) dst_sel:DWORD dst_unused:UNUSED_PAD src0_sel:DWORD src1_sel:WORD_0
	v_ashrrev_i32_e32 v5, 6, v4
	v_lshlrev_b32_e32 v3, 5, v3
	v_lshlrev_b32_e32 v5, 2, v5
	v_and_b32_e32 v6, 0xffffffc0, v3
	v_add3_u32 v5, s81, v5, v6
	ds_read_b32 v5, v5
	s_waitcnt lgkmcnt(1)
	v_lshl_add_u32 v194, v0, 1, v2
	v_and_b32_e32 v2, 0xc0, v4
	v_sub_u32_e32 v1, v1, v2
	v_and_b32_e32 v0, 32, v3
	v_ashrrev_i16_sdwa v1, v193, sext(v1) dst_sel:DWORD dst_unused:UNUSED_PAD src0_sel:DWORD src1_sel:BYTE_0
	v_add_u32_sdwa v0, v0, sext(v1) dst_sel:DWORD dst_unused:UNUSED_PAD src0_sel:DWORD src1_sel:WORD_0
	s_waitcnt lgkmcnt(0)
	v_lshl_add_u32 v196, v0, 1, v5

; __device__ __forceinline__ unsigned pk4_fp8(float a, float b, float c, float d) { int w = __builtin_amdgcn_cvt_pk_fp8_f32(a, b, 0, false); w = __builtin_amdgcn_cvt_pk_fp8_f32(c, d, w, true); return (unsigned)w; }
;     __device__ __forceinline__ void operator()(const f32x4 (&acc)[2][2][4][2], const Unit& u, int wr, int wc, int fr, int fq) const {
;         const int row0 = u.pm * BM + wr * 64 + fr, c0 = u.pn * HALF + wc * 32 + 8 * fq;
;         const float* bp = bgu + (size_t)u.aux * 2048 + c0;
;         const f32x4 bg0 = *(const f32x4*)(bp), bg1 = *(const f32x4*)(bp + 4), bu0 = *(const f32x4*)(bp + 1024), bu1 = *(const f32x4*)(bp + 1028);
; #pragma unroll
;         for (int ai = 0; ai < 2; ++ai)
; #pragma unroll
;             for (int mp = 0; mp < 2; ++mp) {
;                 u32x2 wq[2];
; #pragma unroll
;                 for (int mi = 0; mi < 2; ++mi) { const int m = 2 * mp + mi;
;                     const f32x4 g0 = acc[ai][0][m][0] * ascale + bg0, g1 = acc[ai][0][m][1] * ascale + bg1, u0 = acc[ai][1][m][0] * ascale + bu0, u1 = acc[ai][1][m][1] * ascale + bu1;
;                     float r[8];
; #pragma unroll
;                     for (int j = 0; j < 4; ++j) {
;                         float gg = fminf(g0[j], 7.f), uu = fminf(fmaxf(u0[j], -7.f), 7.f); r[j] = 4.f * (uu + 1.f) * gg * __builtin_amdgcn_rcpf(1.f + __expf(-1.702f * gg));
;                         gg = fminf(g1[j], 7.f); uu = fminf(fmaxf(u1[j], -7.f), 7.f); r[4 + j] = 4.f * (uu + 1.f) * gg * __builtin_amdgcn_rcpf(1.f + __expf(-1.702f * gg));
;                     }
;                     wq[mi].x = pk4_fp8(r[0], r[1], r[2], r[3]); wq[mi].y = pk4_fp8(r[4], r[5], r[6], r[7]); }
;                 *(u32x4*)(act + (size_t)(row0 + ai * HALF + (2 * mp + (fq & 1)) * 16) * EFF + (c0 - 8 * (fq & 1))) = widen16(wq[0], wq[1]);
.LBB0_2537:
	v_mov_b32_e32 v18, v192
	s_lshl_b32 s26, s26, 7
	v_lshrrev_b32_e32 v0, 1, v18
	s_ashr_i32 s37, s36, 31
	s_lshl_b32 s38, s77, 8
	v_and_or_b32 v0, v0, 24, s26
	s_lshl_b64 s[36:37], s[36:37], 13
	v_or_b32_e32 v16, s64, v0
	s_add_u32 s36, s61, s36
	s_addc_u32 s37, s62, s37
	v_ashrrev_i32_e32 v17, 31, v16
	v_lshl_add_u64 v[0:1], v[16:17], 2, s[36:37]
	v_add_co_u32_e32 v2, vcc, s73, v0
	v_bfe_u32 v17, v18, 4, 1
	s_nop 0
	v_addc_co_u32_e32 v3, vcc, 0, v1, vcc
	v_lshl_add_u64 v[0:1], v[0:1], 0, s[16:17]
	v_lshlrev_b32_e32 v19, 3, v17
	v_sub_u32_e32 v16, v16, v19
	s_add_i32 s38, s38, s63
	v_and_or_b32 v18, v18, 15, s38
	v_lshl_or_b32 v18, v17, 4, v18
	v_ashrrev_i32_e32 v17, 31, v16
	s_andn2_b64 vcc, exec, s[24:25]
	s_mov_b64 s[24:25], -1
	s_mov_b32 s98, 0x3a000000
	s_mov_b32 s99, 0xbfd9db23
	s_mov_b32 s100, 0x3fb8aa3b
	s_mov_b32 s101, 0
	v_ashrrev_i32_e32 v19, 31, v18
	v_lshlrev_b64 v[48:49], 10, v[18:19]
	v_lshl_add_u64 v[48:49], s[12:13], 0, v[48:49]
	v_lshl_add_u64 v[48:49], v[48:49], 0, v[16:17]
	v_mov_b32_e32 v52, 0x8000
	v_mov_b32_e32 v53, 0
	v_mov_b32_e32 v54, 0x20000
	v_mov_b32_e32 v55, 0
	v_pk_fma_f32 v[24:25], v[188:189], s[98:99], v[212:213] op_sel_hi:[1,0,1]
	v_pk_fma_f32 v[26:27], v[190:191], s[98:99], v[214:215] op_sel_hi:[1,0,1]
	v_pk_fma_f32 v[28:29], v[184:185], s[98:99], v[216:217] op_sel_hi:[1,0,1]
	v_pk_fma_f32 v[30:31], v[186:187], s[98:99], v[218:219] op_sel_hi:[1,0,1]
	v_pk_fma_f32 v[40:41], v[180:181], s[98:99], v[220:221] op_sel_hi:[1,0,1]
	v_pk_fma_f32 v[42:43], v[182:183], s[98:99], v[222:223] op_sel_hi:[1,0,1]
	v_pk_fma_f32 v[44:45], v[176:177], s[98:99], v[224:225] op_sel_hi:[1,0,1]
	v_pk_fma_f32 v[46:47], v[178:179], s[98:99], v[226:227] op_sel_hi:[1,0,1]
	v_min_f32_e32 v24, 0x40e00000, v24
	v_min_f32_e32 v25, 0x40e00000, v25
	v_min_f32_e32 v26, 0x40e00000, v26
	v_min_f32_e32 v27, 0x40e00000, v27
	v_min_f32_e32 v28, 0x40e00000, v28
	v_min_f32_e32 v29, 0x40e00000, v29
	v_min_f32_e32 v30, 0x40e00000, v30
	v_min_f32_e32 v31, 0x40e00000, v31
	v_med3_f32 v40, v40, s74, v203
	v_med3_f32 v41, v41, s74, v203
	v_med3_f32 v42, v42, s74, v203
	v_med3_f32 v43, v43, s74, v203
	v_med3_f32 v44, v44, s74, v203
	v_med3_f32 v45, v45, s74, v203
	v_med3_f32 v46, v46, s74, v203
	v_med3_f32 v47, v47, s74, v203
	v_pk_mul_f32 v[32:33], v[24:25], s[98:99] op_sel:[0,1] op_sel_hi:[1,1]
	v_pk_mul_f32 v[34:35], v[26:27], s[98:99] op_sel:[0,1] op_sel_hi:[1,1]
	v_pk_mul_f32 v[36:37], v[28:29], s[98:99] op_sel:[0,1] op_sel_hi:[1,1]
	v_pk_mul_f32 v[38:39], v[30:31], s[98:99] op_sel:[0,1] op_sel_hi:[1,1]
	v_pk_mul_f32 v[32:33], v[32:33], s[100:101] op_sel_hi:[1,0]
	v_pk_mul_f32 v[34:35], v[34:35], s[100:101] op_sel_hi:[1,0]
	v_pk_mul_f32 v[36:37], v[36:37], s[100:101] op_sel_hi:[1,0]
	v_pk_mul_f32 v[38:39], v[38:39], s[100:101] op_sel_hi:[1,0]
	v_pk_fma_f32 v[40:41], v[40:41], 4.0, 4.0 op_sel_hi:[1,0,0]
	v_pk_fma_f32 v[42:43], v[42:43], 4.0, 4.0 op_sel_hi:[1,0,0]
	v_pk_fma_f32 v[44:45], v[44:45], 4.0, 4.0 op_sel_hi:[1,0,0]
	v_pk_fma_f32 v[46:47], v[46:47], 4.0, 4.0 op_sel_hi:[1,0,0]
	v_exp_f32_e32 v32, v32
	v_exp_f32_e32 v33, v33
	v_exp_f32_e32 v34, v34
	v_exp_f32_e32 v35, v35
	v_exp_f32_e32 v36, v36
	v_exp_f32_e32 v37, v37
	v_exp_f32_e32 v38, v38
	v_exp_f32_e32 v39, v39
	v_pk_mul_f32 v[40:41], v[24:25], v[40:41]
	v_pk_mul_f32 v[42:43], v[26:27], v[42:43]
	v_pk_mul_f32 v[44:45], v[28:29], v[44:45]
	v_pk_mul_f32 v[46:47], v[30:31], v[46:47]
	v_pk_add_f32 v[32:33], v[32:33], 1.0 op_sel_hi:[1,0]
	v_pk_add_f32 v[34:35], v[34:35], 1.0 op_sel_hi:[1,0]
	v_pk_add_f32 v[36:37], v[36:37], 1.0 op_sel_hi:[1,0]
	v_pk_add_f32 v[38:39], v[38:39], 1.0 op_sel_hi:[1,0]
	v_rcp_f32_e32 v32, v32
	v_rcp_f32_e32 v33, v33
	v_rcp_f32_e32 v34, v34
	v_rcp_f32_e32 v35, v35
	v_rcp_f32_e32 v36, v36
	v_rcp_f32_e32 v37, v37
	v_rcp_f32_e32 v38, v38
	v_rcp_f32_e32 v39, v39
	v_pk_mul_f32 v[40:41], v[32:33], v[40:41]
	v_pk_mul_f32 v[42:43], v[34:35], v[42:43]
	v_pk_mul_f32 v[44:45], v[36:37], v[44:45]
	v_pk_mul_f32 v[46:47], v[38:39], v[46:47]
	v_cvt_pk_fp8_f32 v20, v40, v41
	v_cvt_pk_fp8_f32 v21, v44, v45
	v_cvt_pk_fp8_f32 v20, v42, v43 op_sel:[0,0,1]
	v_cvt_pk_fp8_f32 v21, v46, v47 op_sel:[0,0,1]
	v_pk_fma_f32 v[24:25], v[172:173], s[98:99], v[212:213] op_sel_hi:[1,0,1]
	v_pk_fma_f32 v[26:27], v[174:175], s[98:99], v[214:215] op_sel_hi:[1,0,1]
	v_pk_fma_f32 v[28:29], v[168:169], s[98:99], v[216:217] op_sel_hi:[1,0,1]
	v_pk_fma_f32 v[30:31], v[170:171], s[98:99], v[218:219] op_sel_hi:[1,0,1]
	v_pk_fma_f32 v[40:41], v[164:165], s[98:99], v[220:221] op_sel_hi:[1,0,1]
	v_pk_fma_f32 v[42:43], v[166:167], s[98:99], v[222:223] op_sel_hi:[1,0,1]
	v_pk_fma_f32 v[44:45], v[160:161], s[98:99], v[224:225] op_sel_hi:[1,0,1]
	v_pk_fma_f32 v[46:47], v[162:163], s[98:99], v[226:227] op_sel_hi:[1,0,1]
	v_min_f32_e32 v24, 0x40e00000, v24
	v_min_f32_e32 v25, 0x40e00000, v25
	v_min_f32_e32 v26, 0x40e00000, v26
	v_min_f32_e32 v27, 0x40e00000, v27
	v_min_f32_e32 v28, 0x40e00000, v28
	v_min_f32_e32 v29, 0x40e00000, v29
	v_min_f32_e32 v30, 0x40e00000, v30
	v_min_f32_e32 v31, 0x40e00000, v31
	v_med3_f32 v40, v40, s74, v203
	v_med3_f32 v41, v41, s74, v203
	v_med3_f32 v42, v42, s74, v203
	v_med3_f32 v43, v43, s74, v203
	v_med3_f32 v44, v44, s74, v203
	v_med3_f32 v45, v45, s74, v203
	v_med3_f32 v46, v46, s74, v203
	v_med3_f32 v47, v47, s74, v203
	v_pk_mul_f32 v[32:33], v[24:25], s[98:99] op_sel:[0,1] op_sel_hi:[1,1]
	v_pk_mul_f32 v[34:35], v[26:27], s[98:99] op_sel:[0,1] op_sel_hi:[1,1]
	v_pk_mul_f32 v[36:37], v[28:29], s[98:99] op_sel:[0,1] op_sel_hi:[1,1]
	v_pk_mul_f32 v[38:39], v[30:31], s[98:99] op_sel:[0,1] op_sel_hi:[1,1]
	v_pk_mul_f32 v[32:33], v[32:33], s[100:101] op_sel_hi:[1,0]
; __device__ __forceinline__ unsigned pk4_fp8(float a, float b, float c, float d) { int w = __builtin_amdgcn_cvt_pk_fp8_f32(a, b, 0, false); w = __builtin_amdgcn_cvt_pk_fp8_f32(c, d, w, true); return (unsigned)w; }
;     __device__ __forceinline__ void operator()(const f32x4 (&acc)[2][2][4][2], const Unit& u, int wr, int wc, int fr, int fq) const {
;     ...
;         for (int ai = 0; ai < 2; ++ai)
; #pragma unroll
;             for (int mp = 0; mp < 2; ++mp) {
;                 u32x2 wq[2];
; #pragma unroll
;                 for (int mi = 0; mi < 2; ++mi) { const int m = 2 * mp + mi;
;                     const f32x4 g0 = acc[ai][0][m][0] * ascale + bg0, g1 = acc[ai][0][m][1] * ascale + bg1, u0 = acc[ai][1][m][0] * ascale + bu0, u1 = acc[ai][1][m][1] * ascale + bu1;
;                     float r[8];
; #pragma unroll
;                     for (int j = 0; j < 4; ++j) {
;                         float gg = fminf(g0[j], 7.f), uu = fminf(fmaxf(u0[j], -7.f), 7.f); r[j] = 4.f * (uu + 1.f) * gg * __builtin_amdgcn_rcpf(1.f + __expf(-1.702f * gg));
;                         gg = fminf(g1[j], 7.f); uu = fminf(fmaxf(u1[j], -7.f), 7.f); r[4 + j] = 4.f * (uu + 1.f) * gg * __builtin_amdgcn_rcpf(1.f + __expf(-1.702f * gg));
;                     }
;                     wq[mi].x = pk4_fp8(r[0], r[1], r[2], r[3]); wq[mi].y = pk4_fp8(r[4], r[5], r[6], r[7]); }
;                 *(u32x4*)(act + (size_t)(row0 + ai * HALF + (2 * mp + (fq & 1)) * 16) * EFF + (c0 - 8 * (fq & 1))) = widen16(wq[0], wq[1]);
;             }
	v_pk_mul_f32 v[34:35], v[34:35], s[100:101] op_sel_hi:[1,0]
	v_pk_mul_f32 v[36:37], v[36:37], s[100:101] op_sel_hi:[1,0]
	v_pk_mul_f32 v[38:39], v[38:39], s[100:101] op_sel_hi:[1,0]
	v_pk_fma_f32 v[40:41], v[40:41], 4.0, 4.0 op_sel_hi:[1,0,0]
	v_pk_fma_f32 v[42:43], v[42:43], 4.0, 4.0 op_sel_hi:[1,0,0]
	v_pk_fma_f32 v[44:45], v[44:45], 4.0, 4.0 op_sel_hi:[1,0,0]
	v_pk_fma_f32 v[46:47], v[46:47], 4.0, 4.0 op_sel_hi:[1,0,0]
	v_exp_f32_e32 v32, v32
	v_exp_f32_e32 v33, v33
	v_exp_f32_e32 v34, v34
	v_exp_f32_e32 v35, v35
	v_exp_f32_e32 v36, v36
	v_exp_f32_e32 v37, v37
	v_exp_f32_e32 v38, v38
	v_exp_f32_e32 v39, v39
	v_pk_mul_f32 v[40:41], v[24:25], v[40:41]
	v_pk_mul_f32 v[42:43], v[26:27], v[42:43]
	v_pk_mul_f32 v[44:45], v[28:29], v[44:45]
	v_pk_mul_f32 v[46:47], v[30:31], v[46:47]
	v_pk_add_f32 v[32:33], v[32:33], 1.0 op_sel_hi:[1,0]
	v_pk_add_f32 v[34:35], v[34:35], 1.0 op_sel_hi:[1,0]
	v_pk_add_f32 v[36:37], v[36:37], 1.0 op_sel_hi:[1,0]
	v_pk_add_f32 v[38:39], v[38:39], 1.0 op_sel_hi:[1,0]
	v_rcp_f32_e32 v32, v32
	v_rcp_f32_e32 v33, v33
	v_rcp_f32_e32 v34, v34
	v_rcp_f32_e32 v35, v35
	v_rcp_f32_e32 v36, v36
	v_rcp_f32_e32 v37, v37
	v_rcp_f32_e32 v38, v38
	v_rcp_f32_e32 v39, v39
	v_pk_mul_f32 v[40:41], v[32:33], v[40:41]
	v_pk_mul_f32 v[42:43], v[34:35], v[42:43]
	v_pk_mul_f32 v[44:45], v[36:37], v[44:45]
	v_pk_mul_f32 v[46:47], v[38:39], v[46:47]
	v_cvt_pk_fp8_f32 v22, v40, v41
	v_cvt_pk_fp8_f32 v23, v44, v45
	v_cvt_pk_fp8_f32 v22, v42, v43 op_sel:[0,0,1]
	v_cvt_pk_fp8_f32 v23, v46, v47 op_sel:[0,0,1]
	v_mov_b64_e32 v[50:51], v[48:49]
	s_nop 1
	v_permlane16_swap_b32_e32 v20, v22
	v_permlane16_swap_b32_e32 v21, v23
	global_store_dwordx4 v[50:51], v[20:23], off
	v_pk_fma_f32 v[24:25], v[156:157], s[98:99], v[212:213] op_sel_hi:[1,0,1]
	v_pk_fma_f32 v[26:27], v[158:159], s[98:99], v[214:215] op_sel_hi:[1,0,1]
	v_pk_fma_f32 v[28:29], v[152:153], s[98:99], v[216:217] op_sel_hi:[1,0,1]
	v_pk_fma_f32 v[30:31], v[154:155], s[98:99], v[218:219] op_sel_hi:[1,0,1]
	v_pk_fma_f32 v[40:41], v[148:149], s[98:99], v[220:221] op_sel_hi:[1,0,1]
	v_pk_fma_f32 v[42:43], v[150:151], s[98:99], v[222:223] op_sel_hi:[1,0,1]
	v_pk_fma_f32 v[44:45], v[144:145], s[98:99], v[224:225] op_sel_hi:[1,0,1]
	v_pk_fma_f32 v[46:47], v[146:147], s[98:99], v[226:227] op_sel_hi:[1,0,1]
	v_min_f32_e32 v24, 0x40e00000, v24
	v_min_f32_e32 v25, 0x40e00000, v25
	v_min_f32_e32 v26, 0x40e00000, v26
	v_min_f32_e32 v27, 0x40e00000, v27
	v_min_f32_e32 v28, 0x40e00000, v28
	v_min_f32_e32 v29, 0x40e00000, v29
	v_min_f32_e32 v30, 0x40e00000, v30
	v_min_f32_e32 v31, 0x40e00000, v31
	v_med3_f32 v40, v40, s74, v203
	v_med3_f32 v41, v41, s74, v203
	v_med3_f32 v42, v42, s74, v203
	v_med3_f32 v43, v43, s74, v203
	v_med3_f32 v44, v44, s74, v203
	v_med3_f32 v45, v45, s74, v203
	v_med3_f32 v46, v46, s74, v203
	v_med3_f32 v47, v47, s74, v203
	v_pk_mul_f32 v[32:33], v[24:25], s[98:99] op_sel:[0,1] op_sel_hi:[1,1]
	v_pk_mul_f32 v[34:35], v[26:27], s[98:99] op_sel:[0,1] op_sel_hi:[1,1]
	v_pk_mul_f32 v[36:37], v[28:29], s[98:99] op_sel:[0,1] op_sel_hi:[1,1]
	v_pk_mul_f32 v[38:39], v[30:31], s[98:99] op_sel:[0,1] op_sel_hi:[1,1]
	v_pk_mul_f32 v[32:33], v[32:33], s[100:101] op_sel_hi:[1,0]
	v_pk_mul_f32 v[34:35], v[34:35], s[100:101] op_sel_hi:[1,0]
	v_pk_mul_f32 v[36:37], v[36:37], s[100:101] op_sel_hi:[1,0]
	v_pk_mul_f32 v[38:39], v[38:39], s[100:101] op_sel_hi:[1,0]
	v_pk_fma_f32 v[40:41], v[40:41], 4.0, 4.0 op_sel_hi:[1,0,0]
	v_pk_fma_f32 v[42:43], v[42:43], 4.0, 4.0 op_sel_hi:[1,0,0]
	v_pk_fma_f32 v[44:45], v[44:45], 4.0, 4.0 op_sel_hi:[1,0,0]
	v_pk_fma_f32 v[46:47], v[46:47], 4.0, 4.0 op_sel_hi:[1,0,0]
	v_exp_f32_e32 v32, v32
	v_exp_f32_e32 v33, v33
	v_exp_f32_e32 v34, v34
	v_exp_f32_e32 v35, v35
	v_exp_f32_e32 v36, v36
	v_exp_f32_e32 v37, v37
	v_exp_f32_e32 v38, v38
	v_exp_f32_e32 v39, v39
	v_pk_mul_f32 v[40:41], v[24:25], v[40:41]
	v_pk_mul_f32 v[42:43], v[26:27], v[42:43]
	v_pk_mul_f32 v[44:45], v[28:29], v[44:45]
	v_pk_mul_f32 v[46:47], v[30:31], v[46:47]
	v_pk_add_f32 v[32:33], v[32:33], 1.0 op_sel_hi:[1,0]
	v_pk_add_f32 v[34:35], v[34:35], 1.0 op_sel_hi:[1,0]
	v_pk_add_f32 v[36:37], v[36:37], 1.0 op_sel_hi:[1,0]
	v_pk_add_f32 v[38:39], v[38:39], 1.0 op_sel_hi:[1,0]
	v_rcp_f32_e32 v32, v32
	v_rcp_f32_e32 v33, v33
	v_rcp_f32_e32 v34, v34
	v_rcp_f32_e32 v35, v35
	v_rcp_f32_e32 v36, v36
	v_rcp_f32_e32 v37, v37
	v_rcp_f32_e32 v38, v38
	v_rcp_f32_e32 v39, v39
	v_pk_mul_f32 v[40:41], v[32:33], v[40:41]
	v_pk_mul_f32 v[42:43], v[34:35], v[42:43]
	v_pk_mul_f32 v[44:45], v[36:37], v[44:45]
	v_pk_mul_f32 v[46:47], v[38:39], v[46:47]
	v_cvt_pk_fp8_f32 v20, v40, v41
	v_cvt_pk_fp8_f32 v21, v44, v45
	v_cvt_pk_fp8_f32 v20, v42, v43 op_sel:[0,0,1]
	v_cvt_pk_fp8_f32 v21, v46, v47 op_sel:[0,0,1]
	v_pk_fma_f32 v[24:25], v[140:141], s[98:99], v[212:213] op_sel_hi:[1,0,1]
	v_pk_fma_f32 v[26:27], v[142:143], s[98:99], v[214:215] op_sel_hi:[1,0,1]
	v_pk_fma_f32 v[28:29], v[136:137], s[98:99], v[216:217] op_sel_hi:[1,0,1]
	v_pk_fma_f32 v[30:31], v[138:139], s[98:99], v[218:219] op_sel_hi:[1,0,1]
	v_pk_fma_f32 v[40:41], v[132:133], s[98:99], v[220:221] op_sel_hi:[1,0,1]
	v_pk_fma_f32 v[42:43], v[134:135], s[98:99], v[222:223] op_sel_hi:[1,0,1]
	v_pk_fma_f32 v[44:45], v[128:129], s[98:99], v[224:225] op_sel_hi:[1,0,1]
	v_pk_fma_f32 v[46:47], v[130:131], s[98:99], v[226:227] op_sel_hi:[1,0,1]
	v_min_f32_e32 v24, 0x40e00000, v24
	v_min_f32_e32 v25, 0x40e00000, v25
	v_min_f32_e32 v26, 0x40e00000, v26
	v_min_f32_e32 v27, 0x40e00000, v27
	v_min_f32_e32 v28, 0x40e00000, v28
	v_min_f32_e32 v29, 0x40e00000, v29
	v_min_f32_e32 v30, 0x40e00000, v30
	v_min_f32_e32 v31, 0x40e00000, v31
	v_med3_f32 v40, v40, s74, v203
; __device__ __forceinline__ unsigned pk4_fp8(float a, float b, float c, float d) { int w = __builtin_amdgcn_cvt_pk_fp8_f32(a, b, 0, false); w = __builtin_amdgcn_cvt_pk_fp8_f32(c, d, w, true); return (unsigned)w; }
;     __device__ __forceinline__ void operator()(const f32x4 (&acc)[2][2][4][2], const Unit& u, int wr, int wc, int fr, int fq) const {
;     ...
;         for (int ai = 0; ai < 2; ++ai)
; #pragma unroll
;             for (int mp = 0; mp < 2; ++mp) {
;                 u32x2 wq[2];
; #pragma unroll
;                 for (int mi = 0; mi < 2; ++mi) { const int m = 2 * mp + mi;
;                     const f32x4 g0 = acc[ai][0][m][0] * ascale + bg0, g1 = acc[ai][0][m][1] * ascale + bg1, u0 = acc[ai][1][m][0] * ascale + bu0, u1 = acc[ai][1][m][1] * ascale + bu1;
;                     float r[8];
; #pragma unroll
;                     for (int j = 0; j < 4; ++j) {
;                         float gg = fminf(g0[j], 7.f), uu = fminf(fmaxf(u0[j], -7.f), 7.f); r[j] = 4.f * (uu + 1.f) * gg * __builtin_amdgcn_rcpf(1.f + __expf(-1.702f * gg));
;                         gg = fminf(g1[j], 7.f); uu = fminf(fmaxf(u1[j], -7.f), 7.f); r[4 + j] = 4.f * (uu + 1.f) * gg * __builtin_amdgcn_rcpf(1.f + __expf(-1.702f * gg));
;                     }
;                     wq[mi].x = pk4_fp8(r[0], r[1], r[2], r[3]); wq[mi].y = pk4_fp8(r[4], r[5], r[6], r[7]); }
;                 *(u32x4*)(act + (size_t)(row0 + ai * HALF + (2 * mp + (fq & 1)) * 16) * EFF + (c0 - 8 * (fq & 1))) = widen16(wq[0], wq[1]);
;             }
	v_med3_f32 v41, v41, s74, v203
	v_med3_f32 v42, v42, s74, v203
	v_med3_f32 v43, v43, s74, v203
	v_med3_f32 v44, v44, s74, v203
	v_med3_f32 v45, v45, s74, v203
	v_med3_f32 v46, v46, s74, v203
	v_med3_f32 v47, v47, s74, v203
	v_pk_mul_f32 v[32:33], v[24:25], s[98:99] op_sel:[0,1] op_sel_hi:[1,1]
	v_pk_mul_f32 v[34:35], v[26:27], s[98:99] op_sel:[0,1] op_sel_hi:[1,1]
	v_pk_mul_f32 v[36:37], v[28:29], s[98:99] op_sel:[0,1] op_sel_hi:[1,1]
	v_pk_mul_f32 v[38:39], v[30:31], s[98:99] op_sel:[0,1] op_sel_hi:[1,1]
	v_pk_mul_f32 v[32:33], v[32:33], s[100:101] op_sel_hi:[1,0]
	v_pk_mul_f32 v[34:35], v[34:35], s[100:101] op_sel_hi:[1,0]
	v_pk_mul_f32 v[36:37], v[36:37], s[100:101] op_sel_hi:[1,0]
	v_pk_mul_f32 v[38:39], v[38:39], s[100:101] op_sel_hi:[1,0]
	v_pk_fma_f32 v[40:41], v[40:41], 4.0, 4.0 op_sel_hi:[1,0,0]
	v_pk_fma_f32 v[42:43], v[42:43], 4.0, 4.0 op_sel_hi:[1,0,0]
	v_pk_fma_f32 v[44:45], v[44:45], 4.0, 4.0 op_sel_hi:[1,0,0]
	v_pk_fma_f32 v[46:47], v[46:47], 4.0, 4.0 op_sel_hi:[1,0,0]
	v_exp_f32_e32 v32, v32
	v_exp_f32_e32 v33, v33
	v_exp_f32_e32 v34, v34
	v_exp_f32_e32 v35, v35
	v_exp_f32_e32 v36, v36
	v_exp_f32_e32 v37, v37
	v_exp_f32_e32 v38, v38
	v_exp_f32_e32 v39, v39
	v_pk_mul_f32 v[40:41], v[24:25], v[40:41]
	v_pk_mul_f32 v[42:43], v[26:27], v[42:43]
	v_pk_mul_f32 v[44:45], v[28:29], v[44:45]
	v_pk_mul_f32 v[46:47], v[30:31], v[46:47]
	v_pk_add_f32 v[32:33], v[32:33], 1.0 op_sel_hi:[1,0]
	v_pk_add_f32 v[34:35], v[34:35], 1.0 op_sel_hi:[1,0]
	v_pk_add_f32 v[36:37], v[36:37], 1.0 op_sel_hi:[1,0]
	v_pk_add_f32 v[38:39], v[38:39], 1.0 op_sel_hi:[1,0]
	v_rcp_f32_e32 v32, v32
	v_rcp_f32_e32 v33, v33
	v_rcp_f32_e32 v34, v34
	v_rcp_f32_e32 v35, v35
	v_rcp_f32_e32 v36, v36
	v_rcp_f32_e32 v37, v37
	v_rcp_f32_e32 v38, v38
	v_rcp_f32_e32 v39, v39
	v_pk_mul_f32 v[40:41], v[32:33], v[40:41]
	v_pk_mul_f32 v[42:43], v[34:35], v[42:43]
	v_pk_mul_f32 v[44:45], v[36:37], v[44:45]
	v_pk_mul_f32 v[46:47], v[38:39], v[46:47]
	v_cvt_pk_fp8_f32 v22, v40, v41
	v_cvt_pk_fp8_f32 v23, v44, v45
	v_cvt_pk_fp8_f32 v22, v42, v43 op_sel:[0,0,1]
	v_cvt_pk_fp8_f32 v23, v46, v47 op_sel:[0,0,1]
	v_lshl_add_u64 v[50:51], v[48:49], 0, v[52:53]
	s_nop 1
	v_permlane16_swap_b32_e32 v20, v22
	v_permlane16_swap_b32_e32 v21, v23
	global_store_dwordx4 v[50:51], v[20:23], off
	v_pk_fma_f32 v[24:25], v[124:125], s[98:99], v[212:213] op_sel_hi:[1,0,1]
	v_pk_fma_f32 v[26:27], v[126:127], s[98:99], v[214:215] op_sel_hi:[1,0,1]
	v_pk_fma_f32 v[28:29], v[120:121], s[98:99], v[216:217] op_sel_hi:[1,0,1]
	v_pk_fma_f32 v[30:31], v[122:123], s[98:99], v[218:219] op_sel_hi:[1,0,1]
	v_pk_fma_f32 v[40:41], v[116:117], s[98:99], v[220:221] op_sel_hi:[1,0,1]
	v_pk_fma_f32 v[42:43], v[118:119], s[98:99], v[222:223] op_sel_hi:[1,0,1]
	v_pk_fma_f32 v[44:45], v[112:113], s[98:99], v[224:225] op_sel_hi:[1,0,1]
	v_pk_fma_f32 v[46:47], v[114:115], s[98:99], v[226:227] op_sel_hi:[1,0,1]
	v_min_f32_e32 v24, 0x40e00000, v24
	v_min_f32_e32 v25, 0x40e00000, v25
	v_min_f32_e32 v26, 0x40e00000, v26
	v_min_f32_e32 v27, 0x40e00000, v27
	v_min_f32_e32 v28, 0x40e00000, v28
	v_min_f32_e32 v29, 0x40e00000, v29
	v_min_f32_e32 v30, 0x40e00000, v30
	v_min_f32_e32 v31, 0x40e00000, v31
	v_med3_f32 v40, v40, s74, v203
	v_med3_f32 v41, v41, s74, v203
	v_med3_f32 v42, v42, s74, v203
	v_med3_f32 v43, v43, s74, v203
	v_med3_f32 v44, v44, s74, v203
	v_med3_f32 v45, v45, s74, v203
	v_med3_f32 v46, v46, s74, v203
	v_med3_f32 v47, v47, s74, v203
	v_pk_mul_f32 v[32:33], v[24:25], s[98:99] op_sel:[0,1] op_sel_hi:[1,1]
	v_pk_mul_f32 v[34:35], v[26:27], s[98:99] op_sel:[0,1] op_sel_hi:[1,1]
	v_pk_mul_f32 v[36:37], v[28:29], s[98:99] op_sel:[0,1] op_sel_hi:[1,1]
	v_pk_mul_f32 v[38:39], v[30:31], s[98:99] op_sel:[0,1] op_sel_hi:[1,1]
	v_pk_mul_f32 v[32:33], v[32:33], s[100:101] op_sel_hi:[1,0]
	v_pk_mul_f32 v[34:35], v[34:35], s[100:101] op_sel_hi:[1,0]
	v_pk_mul_f32 v[36:37], v[36:37], s[100:101] op_sel_hi:[1,0]
	v_pk_mul_f32 v[38:39], v[38:39], s[100:101] op_sel_hi:[1,0]
	v_pk_fma_f32 v[40:41], v[40:41], 4.0, 4.0 op_sel_hi:[1,0,0]
	v_pk_fma_f32 v[42:43], v[42:43], 4.0, 4.0 op_sel_hi:[1,0,0]
	v_pk_fma_f32 v[44:45], v[44:45], 4.0, 4.0 op_sel_hi:[1,0,0]
	v_pk_fma_f32 v[46:47], v[46:47], 4.0, 4.0 op_sel_hi:[1,0,0]
	v_exp_f32_e32 v32, v32
	v_exp_f32_e32 v33, v33
	v_exp_f32_e32 v34, v34
	v_exp_f32_e32 v35, v35
	v_exp_f32_e32 v36, v36
	v_exp_f32_e32 v37, v37
	v_exp_f32_e32 v38, v38
	v_exp_f32_e32 v39, v39
	v_pk_mul_f32 v[40:41], v[24:25], v[40:41]
	v_pk_mul_f32 v[42:43], v[26:27], v[42:43]
	v_pk_mul_f32 v[44:45], v[28:29], v[44:45]
	v_pk_mul_f32 v[46:47], v[30:31], v[46:47]
	v_pk_add_f32 v[32:33], v[32:33], 1.0 op_sel_hi:[1,0]
	v_pk_add_f32 v[34:35], v[34:35], 1.0 op_sel_hi:[1,0]
	v_pk_add_f32 v[36:37], v[36:37], 1.0 op_sel_hi:[1,0]
	v_pk_add_f32 v[38:39], v[38:39], 1.0 op_sel_hi:[1,0]
	v_rcp_f32_e32 v32, v32
	v_rcp_f32_e32 v33, v33
	v_rcp_f32_e32 v34, v34
	v_rcp_f32_e32 v35, v35
	v_rcp_f32_e32 v36, v36
	v_rcp_f32_e32 v37, v37
	v_rcp_f32_e32 v38, v38
	v_rcp_f32_e32 v39, v39
	v_pk_mul_f32 v[40:41], v[32:33], v[40:41]
	v_pk_mul_f32 v[42:43], v[34:35], v[42:43]
	v_pk_mul_f32 v[44:45], v[36:37], v[44:45]
	v_pk_mul_f32 v[46:47], v[38:39], v[46:47]
	v_cvt_pk_fp8_f32 v20, v40, v41
	v_cvt_pk_fp8_f32 v21, v44, v45
	v_cvt_pk_fp8_f32 v20, v42, v43 op_sel:[0,0,1]
	v_cvt_pk_fp8_f32 v21, v46, v47 op_sel:[0,0,1]
	v_pk_fma_f32 v[24:25], v[108:109], s[98:99], v[212:213] op_sel_hi:[1,0,1]
	v_pk_fma_f32 v[26:27], v[110:111], s[98:99], v[214:215] op_sel_hi:[1,0,1]
	v_pk_fma_f32 v[28:29], v[104:105], s[98:99], v[216:217] op_sel_hi:[1,0,1]
	v_pk_fma_f32 v[30:31], v[106:107], s[98:99], v[218:219] op_sel_hi:[1,0,1]
	v_pk_fma_f32 v[40:41], v[100:101], s[98:99], v[220:221] op_sel_hi:[1,0,1]
; __device__ __forceinline__ unsigned pk4_fp8(float a, float b, float c, float d) { int w = __builtin_amdgcn_cvt_pk_fp8_f32(a, b, 0, false); w = __builtin_amdgcn_cvt_pk_fp8_f32(c, d, w, true); return (unsigned)w; }
;     __device__ __forceinline__ void operator()(const f32x4 (&acc)[2][2][4][2], const Unit& u, int wr, int wc, int fr, int fq) const {
;     ...
;                     const f32x4 g0 = acc[ai][0][m][0] * ascale + bg0, g1 = acc[ai][0][m][1] * ascale + bg1, u0 = acc[ai][1][m][0] * ascale + bu0, u1 = acc[ai][1][m][1] * ascale + bu1;
;                     float r[8];
; #pragma unroll
;                     for (int j = 0; j < 4; ++j) {
;                         float gg = fminf(g0[j], 7.f), uu = fminf(fmaxf(u0[j], -7.f), 7.f); r[j] = 4.f * (uu + 1.f) * gg * __builtin_amdgcn_rcpf(1.f + __expf(-1.702f * gg));
;                         gg = fminf(g1[j], 7.f); uu = fminf(fmaxf(u1[j], -7.f), 7.f); r[4 + j] = 4.f * (uu + 1.f) * gg * __builtin_amdgcn_rcpf(1.f + __expf(-1.702f * gg));
;                     }
;                     wq[mi].x = pk4_fp8(r[0], r[1], r[2], r[3]); wq[mi].y = pk4_fp8(r[4], r[5], r[6], r[7]); }
;                 *(u32x4*)(act + (size_t)(row0 + ai * HALF + (2 * mp + (fq & 1)) * 16) * EFF + (c0 - 8 * (fq & 1))) = widen16(wq[0], wq[1]);
	v_pk_fma_f32 v[42:43], v[102:103], s[98:99], v[222:223] op_sel_hi:[1,0,1]
	v_pk_fma_f32 v[44:45], v[96:97], s[98:99], v[224:225] op_sel_hi:[1,0,1]
	v_pk_fma_f32 v[46:47], v[98:99], s[98:99], v[226:227] op_sel_hi:[1,0,1]
	v_min_f32_e32 v24, 0x40e00000, v24
	v_min_f32_e32 v25, 0x40e00000, v25
	v_min_f32_e32 v26, 0x40e00000, v26
	v_min_f32_e32 v27, 0x40e00000, v27
	v_min_f32_e32 v28, 0x40e00000, v28
	v_min_f32_e32 v29, 0x40e00000, v29
	v_min_f32_e32 v30, 0x40e00000, v30
	v_min_f32_e32 v31, 0x40e00000, v31
	v_med3_f32 v40, v40, s74, v203
	v_med3_f32 v41, v41, s74, v203
	v_med3_f32 v42, v42, s74, v203
	v_med3_f32 v43, v43, s74, v203
	v_med3_f32 v44, v44, s74, v203
	v_med3_f32 v45, v45, s74, v203
	v_med3_f32 v46, v46, s74, v203
	v_med3_f32 v47, v47, s74, v203
	v_pk_mul_f32 v[32:33], v[24:25], s[98:99] op_sel:[0,1] op_sel_hi:[1,1]
	v_pk_mul_f32 v[34:35], v[26:27], s[98:99] op_sel:[0,1] op_sel_hi:[1,1]
	v_pk_mul_f32 v[36:37], v[28:29], s[98:99] op_sel:[0,1] op_sel_hi:[1,1]
	v_pk_mul_f32 v[38:39], v[30:31], s[98:99] op_sel:[0,1] op_sel_hi:[1,1]
	v_pk_mul_f32 v[32:33], v[32:33], s[100:101] op_sel_hi:[1,0]
	v_pk_mul_f32 v[34:35], v[34:35], s[100:101] op_sel_hi:[1,0]
	v_pk_mul_f32 v[36:37], v[36:37], s[100:101] op_sel_hi:[1,0]
	v_pk_mul_f32 v[38:39], v[38:39], s[100:101] op_sel_hi:[1,0]
	v_pk_fma_f32 v[40:41], v[40:41], 4.0, 4.0 op_sel_hi:[1,0,0]
	v_pk_fma_f32 v[42:43], v[42:43], 4.0, 4.0 op_sel_hi:[1,0,0]
	v_pk_fma_f32 v[44:45], v[44:45], 4.0, 4.0 op_sel_hi:[1,0,0]
	v_pk_fma_f32 v[46:47], v[46:47], 4.0, 4.0 op_sel_hi:[1,0,0]
	v_exp_f32_e32 v32, v32
	v_exp_f32_e32 v33, v33
	v_exp_f32_e32 v34, v34
	v_exp_f32_e32 v35, v35
	v_exp_f32_e32 v36, v36
	v_exp_f32_e32 v37, v37
	v_exp_f32_e32 v38, v38
	v_exp_f32_e32 v39, v39
	v_pk_mul_f32 v[40:41], v[24:25], v[40:41]
	v_pk_mul_f32 v[42:43], v[26:27], v[42:43]
	v_pk_mul_f32 v[44:45], v[28:29], v[44:45]
	v_pk_mul_f32 v[46:47], v[30:31], v[46:47]
	v_pk_add_f32 v[32:33], v[32:33], 1.0 op_sel_hi:[1,0]
	v_pk_add_f32 v[34:35], v[34:35], 1.0 op_sel_hi:[1,0]
	v_pk_add_f32 v[36:37], v[36:37], 1.0 op_sel_hi:[1,0]
	v_pk_add_f32 v[38:39], v[38:39], 1.0 op_sel_hi:[1,0]
	v_rcp_f32_e32 v32, v32
	v_rcp_f32_e32 v33, v33
	v_rcp_f32_e32 v34, v34
	v_rcp_f32_e32 v35, v35
	v_rcp_f32_e32 v36, v36
	v_rcp_f32_e32 v37, v37
	v_rcp_f32_e32 v38, v38
	v_rcp_f32_e32 v39, v39
	v_pk_mul_f32 v[40:41], v[32:33], v[40:41]
	v_pk_mul_f32 v[42:43], v[34:35], v[42:43]
	v_pk_mul_f32 v[44:45], v[36:37], v[44:45]
	v_pk_mul_f32 v[46:47], v[38:39], v[46:47]
	v_cvt_pk_fp8_f32 v22, v40, v41
	v_cvt_pk_fp8_f32 v23, v44, v45
	v_cvt_pk_fp8_f32 v22, v42, v43 op_sel:[0,0,1]
	v_cvt_pk_fp8_f32 v23, v46, v47 op_sel:[0,0,1]
	v_lshl_add_u64 v[50:51], v[48:49], 0, v[54:55]
	s_nop 1
	v_permlane16_swap_b32_e32 v20, v22
	v_permlane16_swap_b32_e32 v21, v23
	global_store_dwordx4 v[50:51], v[20:23], off
	v_pk_fma_f32 v[24:25], v[92:93], s[98:99], v[212:213] op_sel_hi:[1,0,1]
	v_pk_fma_f32 v[26:27], v[94:95], s[98:99], v[214:215] op_sel_hi:[1,0,1]
	v_pk_fma_f32 v[28:29], v[88:89], s[98:99], v[216:217] op_sel_hi:[1,0,1]
	v_pk_fma_f32 v[30:31], v[90:91], s[98:99], v[218:219] op_sel_hi:[1,0,1]
	v_pk_fma_f32 v[40:41], v[84:85], s[98:99], v[220:221] op_sel_hi:[1,0,1]
	v_pk_fma_f32 v[42:43], v[86:87], s[98:99], v[222:223] op_sel_hi:[1,0,1]
	v_pk_fma_f32 v[44:45], v[80:81], s[98:99], v[224:225] op_sel_hi:[1,0,1]
	v_pk_fma_f32 v[46:47], v[82:83], s[98:99], v[226:227] op_sel_hi:[1,0,1]
	v_min_f32_e32 v24, 0x40e00000, v24
	v_min_f32_e32 v25, 0x40e00000, v25
	v_min_f32_e32 v26, 0x40e00000, v26
	v_min_f32_e32 v27, 0x40e00000, v27
	v_min_f32_e32 v28, 0x40e00000, v28
	v_min_f32_e32 v29, 0x40e00000, v29
	v_min_f32_e32 v30, 0x40e00000, v30
	v_min_f32_e32 v31, 0x40e00000, v31
	v_med3_f32 v40, v40, s74, v203
	v_med3_f32 v41, v41, s74, v203
	v_med3_f32 v42, v42, s74, v203
	v_med3_f32 v43, v43, s74, v203
	v_med3_f32 v44, v44, s74, v203
	v_med3_f32 v45, v45, s74, v203
	v_med3_f32 v46, v46, s74, v203
	v_med3_f32 v47, v47, s74, v203
	v_pk_mul_f32 v[32:33], v[24:25], s[98:99] op_sel:[0,1] op_sel_hi:[1,1]
	v_pk_mul_f32 v[34:35], v[26:27], s[98:99] op_sel:[0,1] op_sel_hi:[1,1]
	v_pk_mul_f32 v[36:37], v[28:29], s[98:99] op_sel:[0,1] op_sel_hi:[1,1]
	v_pk_mul_f32 v[38:39], v[30:31], s[98:99] op_sel:[0,1] op_sel_hi:[1,1]
	v_pk_mul_f32 v[32:33], v[32:33], s[100:101] op_sel_hi:[1,0]
	v_pk_mul_f32 v[34:35], v[34:35], s[100:101] op_sel_hi:[1,0]
	v_pk_mul_f32 v[36:37], v[36:37], s[100:101] op_sel_hi:[1,0]
	v_pk_mul_f32 v[38:39], v[38:39], s[100:101] op_sel_hi:[1,0]
	v_pk_fma_f32 v[40:41], v[40:41], 4.0, 4.0 op_sel_hi:[1,0,0]
	v_pk_fma_f32 v[42:43], v[42:43], 4.0, 4.0 op_sel_hi:[1,0,0]
; __device__ __forceinline__ unsigned pk4_fp8(float a, float b, float c, float d) { int w = __builtin_amdgcn_cvt_pk_fp8_f32(a, b, 0, false); w = __builtin_amdgcn_cvt_pk_fp8_f32(c, d, w, true); return (unsigned)w; }
;     __device__ __forceinline__ void operator()(const f32x4 (&acc)[2][2][4][2], const Unit& u, int wr, int wc, int fr, int fq) const {
;     ...
;                     const f32x4 g0 = acc[ai][0][m][0] * ascale + bg0, g1 = acc[ai][0][m][1] * ascale + bg1, u0 = acc[ai][1][m][0] * ascale + bu0, u1 = acc[ai][1][m][1] * ascale + bu1;
;                     float r[8];
; #pragma unroll
;                     for (int j = 0; j < 4; ++j) {
;                         float gg = fminf(g0[j], 7.f), uu = fminf(fmaxf(u0[j], -7.f), 7.f); r[j] = 4.f * (uu + 1.f) * gg * __builtin_amdgcn_rcpf(1.f + __expf(-1.702f * gg));
;                         gg = fminf(g1[j], 7.f); uu = fminf(fmaxf(u1[j], -7.f), 7.f); r[4 + j] = 4.f * (uu + 1.f) * gg * __builtin_amdgcn_rcpf(1.f + __expf(-1.702f * gg));
;                     }
;                     wq[mi].x = pk4_fp8(r[0], r[1], r[2], r[3]); wq[mi].y = pk4_fp8(r[4], r[5], r[6], r[7]); }
;                 *(u32x4*)(act + (size_t)(row0 + ai * HALF + (2 * mp + (fq & 1)) * 16) * EFF + (c0 - 8 * (fq & 1))) = widen16(wq[0], wq[1]);
;             }
	v_pk_fma_f32 v[44:45], v[44:45], 4.0, 4.0 op_sel_hi:[1,0,0]
	v_pk_fma_f32 v[46:47], v[46:47], 4.0, 4.0 op_sel_hi:[1,0,0]
	v_exp_f32_e32 v32, v32
	v_exp_f32_e32 v33, v33
	v_exp_f32_e32 v34, v34
	v_exp_f32_e32 v35, v35
	v_exp_f32_e32 v36, v36
	v_exp_f32_e32 v37, v37
	v_exp_f32_e32 v38, v38
	v_exp_f32_e32 v39, v39
	v_pk_mul_f32 v[40:41], v[24:25], v[40:41]
	v_pk_mul_f32 v[42:43], v[26:27], v[42:43]
	v_pk_mul_f32 v[44:45], v[28:29], v[44:45]
	v_pk_mul_f32 v[46:47], v[30:31], v[46:47]
	v_pk_add_f32 v[32:33], v[32:33], 1.0 op_sel_hi:[1,0]
	v_pk_add_f32 v[34:35], v[34:35], 1.0 op_sel_hi:[1,0]
	v_pk_add_f32 v[36:37], v[36:37], 1.0 op_sel_hi:[1,0]
	v_pk_add_f32 v[38:39], v[38:39], 1.0 op_sel_hi:[1,0]
	v_rcp_f32_e32 v32, v32
	v_rcp_f32_e32 v33, v33
	v_rcp_f32_e32 v34, v34
	v_rcp_f32_e32 v35, v35
	v_rcp_f32_e32 v36, v36
	v_rcp_f32_e32 v37, v37
	v_rcp_f32_e32 v38, v38
	v_rcp_f32_e32 v39, v39
	v_pk_mul_f32 v[40:41], v[32:33], v[40:41]
	v_pk_mul_f32 v[42:43], v[34:35], v[42:43]
	v_pk_mul_f32 v[44:45], v[36:37], v[44:45]
	v_pk_mul_f32 v[46:47], v[38:39], v[46:47]
	v_cvt_pk_fp8_f32 v20, v40, v41
	v_cvt_pk_fp8_f32 v21, v44, v45
	v_cvt_pk_fp8_f32 v20, v42, v43 op_sel:[0,0,1]
	v_cvt_pk_fp8_f32 v21, v46, v47 op_sel:[0,0,1]
	v_pk_fma_f32 v[24:25], v[76:77], s[98:99], v[212:213] op_sel_hi:[1,0,1]
	v_pk_fma_f32 v[26:27], v[78:79], s[98:99], v[214:215] op_sel_hi:[1,0,1]
	v_pk_fma_f32 v[28:29], v[72:73], s[98:99], v[216:217] op_sel_hi:[1,0,1]
	v_pk_fma_f32 v[30:31], v[74:75], s[98:99], v[218:219] op_sel_hi:[1,0,1]
	v_pk_fma_f32 v[40:41], v[68:69], s[98:99], v[220:221] op_sel_hi:[1,0,1]
	v_pk_fma_f32 v[42:43], v[70:71], s[98:99], v[222:223] op_sel_hi:[1,0,1]
	v_pk_fma_f32 v[44:45], v[64:65], s[98:99], v[224:225] op_sel_hi:[1,0,1]
	v_pk_fma_f32 v[46:47], v[66:67], s[98:99], v[226:227] op_sel_hi:[1,0,1]
	v_min_f32_e32 v24, 0x40e00000, v24
	v_min_f32_e32 v25, 0x40e00000, v25
	v_min_f32_e32 v26, 0x40e00000, v26
	v_min_f32_e32 v27, 0x40e00000, v27
	v_min_f32_e32 v28, 0x40e00000, v28
	v_min_f32_e32 v29, 0x40e00000, v29
	v_min_f32_e32 v30, 0x40e00000, v30
	v_min_f32_e32 v31, 0x40e00000, v31
	v_med3_f32 v40, v40, s74, v203
	v_med3_f32 v41, v41, s74, v203
	v_med3_f32 v42, v42, s74, v203
	v_med3_f32 v43, v43, s74, v203
	v_med3_f32 v44, v44, s74, v203
	v_med3_f32 v45, v45, s74, v203
	v_med3_f32 v46, v46, s74, v203
	v_med3_f32 v47, v47, s74, v203
	v_pk_mul_f32 v[32:33], v[24:25], s[98:99] op_sel:[0,1] op_sel_hi:[1,1]
	v_pk_mul_f32 v[34:35], v[26:27], s[98:99] op_sel:[0,1] op_sel_hi:[1,1]
	v_pk_mul_f32 v[36:37], v[28:29], s[98:99] op_sel:[0,1] op_sel_hi:[1,1]
	v_pk_mul_f32 v[38:39], v[30:31], s[98:99] op_sel:[0,1] op_sel_hi:[1,1]
	v_pk_mul_f32 v[32:33], v[32:33], s[100:101] op_sel_hi:[1,0]
	v_pk_mul_f32 v[34:35], v[34:35], s[100:101] op_sel_hi:[1,0]
	v_pk_mul_f32 v[36:37], v[36:37], s[100:101] op_sel_hi:[1,0]
	v_pk_mul_f32 v[38:39], v[38:39], s[100:101] op_sel_hi:[1,0]
	v_pk_fma_f32 v[40:41], v[40:41], 4.0, 4.0 op_sel_hi:[1,0,0]
	v_pk_fma_f32 v[42:43], v[42:43], 4.0, 4.0 op_sel_hi:[1,0,0]
	v_pk_fma_f32 v[44:45], v[44:45], 4.0, 4.0 op_sel_hi:[1,0,0]
	v_pk_fma_f32 v[46:47], v[46:47], 4.0, 4.0 op_sel_hi:[1,0,0]
	v_exp_f32_e32 v32, v32
	v_exp_f32_e32 v33, v33
	v_exp_f32_e32 v34, v34
	v_exp_f32_e32 v35, v35
	v_exp_f32_e32 v36, v36
	v_exp_f32_e32 v37, v37
	v_exp_f32_e32 v38, v38
	v_exp_f32_e32 v39, v39
	v_pk_mul_f32 v[40:41], v[24:25], v[40:41]
	v_pk_mul_f32 v[42:43], v[26:27], v[42:43]
	v_pk_mul_f32 v[44:45], v[28:29], v[44:45]
	v_pk_mul_f32 v[46:47], v[30:31], v[46:47]
	v_pk_add_f32 v[32:33], v[32:33], 1.0 op_sel_hi:[1,0]
	v_pk_add_f32 v[34:35], v[34:35], 1.0 op_sel_hi:[1,0]
	v_pk_add_f32 v[36:37], v[36:37], 1.0 op_sel_hi:[1,0]
	v_pk_add_f32 v[38:39], v[38:39], 1.0 op_sel_hi:[1,0]
	v_rcp_f32_e32 v32, v32
	v_rcp_f32_e32 v33, v33
	v_rcp_f32_e32 v34, v34
	v_rcp_f32_e32 v35, v35
	v_rcp_f32_e32 v36, v36
	v_rcp_f32_e32 v37, v37
	v_rcp_f32_e32 v38, v38
	v_rcp_f32_e32 v39, v39
	v_pk_mul_f32 v[40:41], v[32:33], v[40:41]
	v_pk_mul_f32 v[42:43], v[34:35], v[42:43]
	v_pk_mul_f32 v[44:45], v[36:37], v[44:45]
	v_pk_mul_f32 v[46:47], v[38:39], v[46:47]
	v_cvt_pk_fp8_f32 v22, v40, v41
	v_cvt_pk_fp8_f32 v23, v44, v45
	v_cvt_pk_fp8_f32 v22, v42, v43 op_sel:[0,0,1]
	v_cvt_pk_fp8_f32 v23, v46, v47 op_sel:[0,0,1]
	v_lshl_add_u64 v[50:51], v[48:49], 0, v[54:55]
	v_lshl_add_u64 v[50:51], v[50:51], 0, v[52:53]
	s_nop 1
	v_permlane16_swap_b32_e32 v20, v22
	v_permlane16_swap_b32_e32 v21, v23
	global_store_dwordx4 v[50:51], v[20:23], off
	s_cbranch_vccnz .LBB0_2523
	s_andn2_b64 vcc, exec, s[4:5]
	s_cbranch_vccnz .LBB0_2522
	s_barrier
	s_branch .LBB0_2522
